# P5/P8 epilogues: second row-group residual loads issued together with the first group (counted waits +8), group-2 waits dropped
# speedup vs baseline: 1.0063x; 1.0010x over previous
.LBB0_841:
	s_lshl_b32 s6, s50, 8
	v_mov_b32_e32 v114, v174
	s_add_i32 s6, s6, s40
	s_nop 0
	v_and_or_b32 v160, v114, 15, s6
	s_lshl_b32 s6, s49, 8
	v_ashrrev_i32_e32 v112, 1, v114
	s_or_b32 s6, s6, s41
	v_and_b32_e32 v112, -8, v112
	v_add_u32_e32 v156, s6, v112
	v_ashrrev_i32_e32 v157, 31, v156
	v_ashrrev_i32_e32 v161, 31, v160
	v_lshl_add_u64 v[158:159], v[156:157], 1, s[12:13]
	v_lshlrev_b64 v[112:113], 12, v[160:161]
	v_lshl_add_u64 v[196:197], v[158:159], 0, v[112:113]
	global_load_dwordx4 v[188:191], v[196:197], off
	global_load_dwordx4 v[192:195], v[196:197], off offset:256
	v_or_b32_e32 v170, 16, v160
	v_or_b32_e32 v166, 32, v160
	v_or_b32_e32 v162, 48, v160
	v_ashrrev_i32_e32 v171, 31, v170
	v_cmp_gt_u32_e32 vcc, 16, v114
	v_ashrrev_i32_e32 v167, 31, v166
	v_ashrrev_i32_e32 v163, 31, v162
	v_lshlrev_b64 v[114:115], 12, v[170:171]
	v_lshlrev_b64 v[112:113], 11, v[160:161]
	v_lshlrev_b64 v[116:117], 12, v[166:167]
	v_lshlrev_b64 v[118:119], 12, v[162:163]
	v_lshl_add_u64 v[172:173], v[158:159], 0, v[114:115]
	v_lshl_add_u64 v[198:199], v[112:113], 0, v[156:157]
	v_lshl_add_u64 v[168:169], v[158:159], 0, v[116:117]
	v_lshl_add_u64 v[164:165], v[158:159], 0, v[118:119]
	global_load_dwordx4 v[148:151], v[172:173], off
	global_load_dwordx4 v[144:147], v[172:173], off offset:256
	global_load_dwordx4 v[140:143], v[168:169], off
	global_load_dwordx4 v[136:139], v[168:169], off offset:256
	global_load_dwordx4 v[116:119], v[164:165], off
	global_load_dwordx4 v[112:115], v[164:165], off offset:256
	v_add_u32_e32 v248, 0x80, v160
	v_add_u32_e32 v250, 0x90, v160
	v_add_u32_e32 v252, 0xa0, v160
	v_add_u32_e32 v254, 0xb0, v160
	v_ashrrev_i32_e32 v249, 31, v248
	v_ashrrev_i32_e32 v251, 31, v250
	v_ashrrev_i32_e32 v253, 31, v252
	v_ashrrev_i32_e32 v255, 31, v254
	v_lshlrev_b64 v[248:249], 12, v[248:249]
	v_lshlrev_b64 v[250:251], 12, v[250:251]
	v_lshlrev_b64 v[252:253], 12, v[252:253]
	v_lshlrev_b64 v[254:255], 12, v[254:255]
	v_lshl_add_u64 v[240:241], v[158:159], 0, v[248:249]
	v_lshl_add_u64 v[242:243], v[158:159], 0, v[250:251]
	v_lshl_add_u64 v[244:245], v[158:159], 0, v[252:253]
	v_lshl_add_u64 v[246:247], v[158:159], 0, v[254:255]
	global_load_dwordx4 v[208:211], v[240:241], off
	global_load_dwordx4 v[212:215], v[240:241], off offset:256
	global_load_dwordx4 v[216:219], v[242:243], off
	global_load_dwordx4 v[220:223], v[242:243], off offset:256
	global_load_dwordx4 v[224:227], v[244:245], off
	global_load_dwordx4 v[228:231], v[244:245], off offset:256
	global_load_dwordx4 v[232:235], v[246:247], off
	global_load_dwordx4 v[236:239], v[246:247], off offset:256
	s_waitcnt vmcnt(15)
	v_lshlrev_b32_e32 v187, 16, v188
	v_and_b32_e32 v188, 0xffff0000, v188
	v_lshlrev_b32_e32 v200, 16, v189
	v_and_b32_e32 v189, 0xffff0000, v189
	v_lshlrev_b32_e32 v201, 16, v190
	v_and_b32_e32 v190, 0xffff0000, v190
	v_lshlrev_b32_e32 v202, 16, v191
	v_and_b32_e32 v191, 0xffff0000, v191
	v_add_f32_e32 v132, v132, v187
	v_add_f32_e32 v133, v133, v188
	v_add_f32_e32 v134, v134, v200
	v_add_f32_e32 v135, v135, v189
	v_add_f32_e32 v187, v128, v201
	v_add_f32_e32 v188, v129, v190
	v_add_f32_e32 v189, v130, v202
	v_add_f32_e32 v190, v131, v191
	v_mul_f32_e32 v191, v133, v133
	v_mul_f32_e32 v200, v135, v135
	v_cvt_pk_bf16_f32 v128, v132, v133
	v_cvt_pk_bf16_f32 v129, v134, v135
	v_cvt_pk_bf16_f32 v130, v187, v188
	v_cvt_pk_bf16_f32 v131, v189, v190
	v_mul_f32_e32 v203, 0x41c00000, v132
	v_mul_f32_e32 v133, 0x41c00000, v133
	v_mul_f32_e32 v204, 0x41c00000, v134
	v_mul_f32_e32 v135, 0x41c00000, v135
	global_store_dwordx4 v[196:197], v[128:131], off
	v_mul_f32_e32 v201, v188, v188
	v_mul_f32_e32 v202, v190, v190
	v_med3_f32 v128, v203, s42, v186
	v_med3_f32 v129, v133, s42, v186
	v_med3_f32 v130, v204, s42, v186
	v_med3_f32 v131, v135, s42, v186
	v_add_f32_e32 v128, 0x4b400000, v128
	v_add_f32_e32 v129, 0x4b400000, v129
	v_add_f32_e32 v130, 0x4b400000, v130
	v_add_f32_e32 v131, 0x4b400000, v131
	v_mul_f32_e32 v205, 0x41c00000, v187
	v_mul_f32_e32 v188, 0x41c00000, v188
	v_mul_f32_e32 v206, 0x41c00000, v189
	v_mul_f32_e32 v190, 0x41c00000, v190
	v_perm_b32 v128, v129, v128, s43
	v_perm_b32 v129, v131, v130, s43
	v_fmac_f32_e32 v191, v132, v132
	v_fmac_f32_e32 v200, v134, v134
	v_med3_f32 v132, v205, s42, v186
	v_med3_f32 v133, v188, s42, v186
	v_med3_f32 v134, v206, s42, v186
	v_perm_b32 v128, v129, v128, s44
	v_med3_f32 v129, v190, s42, v186
	v_add_f32_e32 v132, 0x4b400000, v132
	v_add_f32_e32 v133, 0x4b400000, v133
	v_add_f32_e32 v134, 0x4b400000, v134
	v_add_f32_e32 v129, 0x4b400000, v129
	v_perm_b32 v130, v133, v132, s43
	v_perm_b32 v129, v129, v134, s43
	v_perm_b32 v129, v129, v130, s44
	v_lshl_add_u64 v[130:131], s[14:15], 0, v[198:199]
	global_store_dwordx2 v[130:131], v[128:129], off
	s_waitcnt vmcnt(16)
	v_lshlrev_b32_e32 v128, 16, v192
	v_add_f32_e32 v124, v124, v128
	v_and_b32_e32 v128, 0xffff0000, v192
	v_add_f32_e32 v125, v125, v128
	v_lshlrev_b32_e32 v128, 16, v193
	v_add_f32_e32 v126, v126, v128
	v_and_b32_e32 v128, 0xffff0000, v193
	v_add_f32_e32 v127, v127, v128
	v_lshlrev_b32_e32 v128, 16, v194
	v_add_f32_e32 v128, v120, v128
	v_and_b32_e32 v120, 0xffff0000, v194
	v_add_f32_e32 v129, v121, v120
	v_lshlrev_b32_e32 v120, 16, v195
	v_add_f32_e32 v132, v122, v120
	v_and_b32_e32 v120, 0xffff0000, v195
	v_add_f32_e32 v133, v123, v120
	v_mul_f32_e32 v120, v125, v125
	v_mul_f32_e32 v121, v127, v127
	v_fmac_f32_e32 v120, v124, v124
	v_fmac_f32_e32 v121, v126, v126
	v_add_f32_e32 v120, v120, v121
	v_mul_f32_e32 v121, v129, v129
	v_mul_f32_e32 v122, v133, v133
	v_fmac_f32_e32 v201, v187, v187
	v_fmac_f32_e32 v202, v189, v189
	v_fmac_f32_e32 v121, v128, v128
	v_fmac_f32_e32 v122, v132, v132
	v_add_f32_e32 v135, v191, v200
	v_add_f32_e32 v187, v201, v202
	v_add_f32_e32 v121, v121, v122
	v_add_f32_e32 v135, v135, v187
	v_add_f32_e32 v120, v120, v121
	v_add_f32_e32 v134, v135, v120
	v_cvt_pk_bf16_f32 v120, v124, v125
	v_cvt_pk_bf16_f32 v121, v126, v127
	v_cvt_pk_bf16_f32 v122, v128, v129
	v_cvt_pk_bf16_f32 v123, v132, v133
	global_store_dwordx4 v[196:197], v[120:123], off offset:256
	s_nop 1
	v_mul_f32_e32 v120, 0x41c00000, v124
	v_mul_f32_e32 v121, 0x41c00000, v125
	v_mul_f32_e32 v122, 0x41c00000, v126
	v_mul_f32_e32 v123, 0x41c00000, v127
	v_med3_f32 v120, v120, s42, v186
	v_med3_f32 v121, v121, s42, v186
	v_med3_f32 v122, v122, s42, v186
	v_med3_f32 v123, v123, s42, v186
	v_add_f32_e32 v120, 0x4b400000, v120
	v_add_f32_e32 v121, 0x4b400000, v121
	v_add_f32_e32 v122, 0x4b400000, v122
	v_add_f32_e32 v123, 0x4b400000, v123
	v_perm_b32 v120, v121, v120, s43
	v_perm_b32 v121, v123, v122, s43
	v_perm_b32 v122, v121, v120, s44
	v_mul_f32_e32 v120, 0x41c00000, v128
	v_mul_f32_e32 v121, 0x41c00000, v129
	v_med3_f32 v120, v120, s42, v186
	v_add_f32_e32 v125, 0x4b400000, v120
	v_med3_f32 v120, v121, s42, v186
	v_add_f32_e32 v126, 0x4b400000, v120
	ds_bpermute_b32 v120, v179, v134
	v_mul_f32_e32 v123, 0x41c00000, v132
	v_mul_f32_e32 v124, 0x41c00000, v133
	v_med3_f32 v121, v123, s42, v186
	v_add_f32_e32 v123, 0x4b400000, v121
	v_med3_f32 v121, v124, s42, v186
	s_waitcnt lgkmcnt(0)
	v_add_f32_e32 v120, v134, v120
	v_add_f32_e32 v124, 0x4b400000, v121
	ds_bpermute_b32 v121, v180, v120
	v_perm_b32 v125, v126, v125, s43
	v_perm_b32 v123, v124, v123, s43
	v_perm_b32 v123, v123, v125, s44
	global_store_dwordx2 v[130:131], v[122:123], off offset:128
	s_and_saveexec_b64 s[22:23], vcc
	s_cbranch_execz .LBB0_843
	s_waitcnt lgkmcnt(0)
	v_add_f32_e32 v120, v120, v121
	v_mul_f32_e32 v120, 0x4b800000, v120
	v_rndne_f32_e32 v120, v120
	v_mul_f32_e64 v121, |v120|, s45
	v_floor_f32_e32 v121, v121
	v_fma_f32 v122, v121, s46, |v120|
	v_cvt_u32_f32_e32 v122, v122
	v_cvt_u32_f32_e32 v121, v121
	v_ashrrev_i32_e32 v123, 31, v120
	v_xor_b32_e32 v120, v122, v123
	v_xor_b32_e32 v121, v121, v123
	v_sub_co_u32_e64 v120, s[6:7], v120, v123
	s_nop 1
	v_subb_co_u32_e64 v121, s[6:7], v121, v123, s[6:7]
	v_lshl_add_u64 v[122:123], v[160:161], 3, s[10:11]
	global_atomic_add_x2 v[122:123], v[120:121], off
.LBB0_843:
	s_or_b64 exec, exec, s[22:23]
	s_waitcnt vmcnt(17)
	v_lshlrev_b32_e32 v122, 16, v148
	v_add_f32_e32 v108, v108, v122
	v_and_b32_e32 v122, 0xffff0000, v148
	v_add_f32_e32 v109, v109, v122
	v_lshlrev_b32_e32 v122, 16, v149
	v_add_f32_e32 v110, v110, v122
	v_and_b32_e32 v122, 0xffff0000, v149
	v_add_f32_e32 v111, v111, v122
	v_lshlrev_b32_e32 v122, 16, v150
	v_add_f32_e32 v122, v104, v122
	v_and_b32_e32 v104, 0xffff0000, v150
	v_add_f32_e32 v123, v105, v104
	v_lshlrev_b32_e32 v104, 16, v151
	v_add_f32_e32 v124, v106, v104
	v_and_b32_e32 v104, 0xffff0000, v151
	v_add_f32_e32 v125, v107, v104
	v_mul_f32_e32 v104, v109, v109
	v_mul_f32_e32 v105, v111, v111
	v_fmac_f32_e32 v104, v108, v108
	v_fmac_f32_e32 v105, v110, v110
	v_add_f32_e32 v104, v104, v105
	v_mul_f32_e32 v105, v123, v123
	v_mul_f32_e32 v106, v125, v125
	v_fmac_f32_e32 v105, v122, v122
	v_fmac_f32_e32 v106, v124, v124
	v_add_f32_e32 v105, v105, v106
	v_add_f32_e32 v126, v104, v105
	v_cvt_pk_bf16_f32 v104, v108, v109
	v_cvt_pk_bf16_f32 v105, v110, v111
	v_cvt_pk_bf16_f32 v106, v122, v123
	v_cvt_pk_bf16_f32 v107, v124, v125
	global_store_dwordx4 v[172:173], v[104:107], off
	s_waitcnt lgkmcnt(0)
	v_lshlrev_b64 v[120:121], 11, v[170:171]
	v_lshl_add_u64 v[120:121], v[120:121], 0, v[156:157]
	v_mul_f32_e32 v104, 0x41c00000, v108
	v_mul_f32_e32 v105, 0x41c00000, v109
	v_mul_f32_e32 v106, 0x41c00000, v110
	v_mul_f32_e32 v107, 0x41c00000, v111
	v_med3_f32 v104, v104, s42, v186
	v_med3_f32 v105, v105, s42, v186
	v_med3_f32 v106, v106, s42, v186
	v_med3_f32 v107, v107, s42, v186
	v_add_f32_e32 v104, 0x4b400000, v104
	v_add_f32_e32 v105, 0x4b400000, v105
	v_add_f32_e32 v106, 0x4b400000, v106
	v_add_f32_e32 v107, 0x4b400000, v107
	v_perm_b32 v104, v105, v104, s43
	v_perm_b32 v105, v107, v106, s43
	v_perm_b32 v104, v105, v104, s44
	v_mul_f32_e32 v105, 0x41c00000, v122
	v_mul_f32_e32 v106, 0x41c00000, v123
	v_mul_f32_e32 v107, 0x41c00000, v124
	v_mul_f32_e32 v108, 0x41c00000, v125
	v_med3_f32 v105, v105, s42, v186
	v_med3_f32 v106, v106, s42, v186
	v_med3_f32 v107, v107, s42, v186
	v_med3_f32 v108, v108, s42, v186
	v_add_f32_e32 v105, 0x4b400000, v105
	v_add_f32_e32 v106, 0x4b400000, v106
	v_add_f32_e32 v107, 0x4b400000, v107
	v_add_f32_e32 v108, 0x4b400000, v108
	v_perm_b32 v105, v106, v105, s43
	v_perm_b32 v106, v108, v107, s43
	v_perm_b32 v105, v106, v105, s44
	v_lshl_add_u64 v[106:107], s[14:15], 0, v[120:121]
	global_store_dwordx2 v[106:107], v[104:105], off
	s_waitcnt vmcnt(18)
	v_lshlrev_b32_e32 v104, 16, v144
	v_add_f32_e32 v100, v100, v104
	v_and_b32_e32 v104, 0xffff0000, v144
	v_add_f32_e32 v101, v101, v104
	v_lshlrev_b32_e32 v104, 16, v145
	v_add_f32_e32 v102, v102, v104
	v_and_b32_e32 v104, 0xffff0000, v145
	v_add_f32_e32 v103, v103, v104
	v_lshlrev_b32_e32 v104, 16, v146
	v_add_f32_e32 v104, v96, v104
	v_and_b32_e32 v96, 0xffff0000, v146
	v_add_f32_e32 v105, v97, v96
	v_lshlrev_b32_e32 v96, 16, v147
	v_add_f32_e32 v108, v98, v96
	v_and_b32_e32 v96, 0xffff0000, v147
	v_add_f32_e32 v109, v99, v96
	v_mul_f32_e32 v96, v101, v101
	v_mul_f32_e32 v97, v103, v103
	v_fmac_f32_e32 v96, v100, v100
	v_fmac_f32_e32 v97, v102, v102
	v_add_f32_e32 v96, v96, v97
	v_mul_f32_e32 v97, v105, v105
	v_mul_f32_e32 v98, v109, v109
	v_fmac_f32_e32 v97, v104, v104
	v_fmac_f32_e32 v98, v108, v108
	v_add_f32_e32 v97, v97, v98
	v_add_f32_e32 v96, v96, v97
	v_add_f32_e32 v110, v126, v96
	v_cvt_pk_bf16_f32 v96, v100, v101
	v_cvt_pk_bf16_f32 v97, v102, v103
	v_cvt_pk_bf16_f32 v98, v104, v105
	v_cvt_pk_bf16_f32 v99, v108, v109
	global_store_dwordx4 v[172:173], v[96:99], off offset:256
	s_nop 1
	v_mul_f32_e32 v96, 0x41c00000, v100
	v_mul_f32_e32 v97, 0x41c00000, v101
	v_mul_f32_e32 v98, 0x41c00000, v102
	v_mul_f32_e32 v99, 0x41c00000, v103
	v_med3_f32 v96, v96, s42, v186
	v_med3_f32 v97, v97, s42, v186
	v_med3_f32 v98, v98, s42, v186
	v_med3_f32 v99, v99, s42, v186
	v_add_f32_e32 v96, 0x4b400000, v96
	v_add_f32_e32 v97, 0x4b400000, v97
	v_add_f32_e32 v98, 0x4b400000, v98
	v_add_f32_e32 v99, 0x4b400000, v99
	v_perm_b32 v96, v97, v96, s43
	v_perm_b32 v97, v99, v98, s43
	v_perm_b32 v98, v97, v96, s44
	v_mul_f32_e32 v96, 0x41c00000, v104
	v_mul_f32_e32 v97, 0x41c00000, v105
	v_med3_f32 v96, v96, s42, v186
	v_add_f32_e32 v101, 0x4b400000, v96
	v_med3_f32 v96, v97, s42, v186
	v_add_f32_e32 v102, 0x4b400000, v96
	ds_bpermute_b32 v96, v179, v110
	v_mul_f32_e32 v99, 0x41c00000, v108
	v_mul_f32_e32 v100, 0x41c00000, v109
	v_med3_f32 v97, v99, s42, v186
	v_add_f32_e32 v99, 0x4b400000, v97
	v_med3_f32 v97, v100, s42, v186
	s_waitcnt lgkmcnt(0)
	v_add_f32_e32 v96, v110, v96
	v_add_f32_e32 v100, 0x4b400000, v97
	ds_bpermute_b32 v97, v180, v96
	v_perm_b32 v101, v102, v101, s43
	v_perm_b32 v99, v100, v99, s43
	v_perm_b32 v99, v99, v101, s44
	global_store_dwordx2 v[106:107], v[98:99], off offset:128
	s_and_saveexec_b64 s[22:23], vcc
	s_cbranch_execz .LBB0_845
	s_waitcnt lgkmcnt(0)
	v_add_f32_e32 v96, v96, v97
	v_mul_f32_e32 v96, 0x4b800000, v96
	v_rndne_f32_e32 v96, v96
	v_mul_f32_e64 v97, |v96|, s45
	v_floor_f32_e32 v97, v97
	v_fma_f32 v98, v97, s46, |v96|
	v_cvt_u32_f32_e32 v98, v98
	v_cvt_u32_f32_e32 v97, v97
	v_ashrrev_i32_e32 v99, 31, v96
	v_xor_b32_e32 v96, v98, v99
	v_xor_b32_e32 v97, v97, v99
	v_sub_co_u32_e64 v96, s[6:7], v96, v99
	s_nop 1
	v_subb_co_u32_e64 v97, s[6:7], v97, v99, s[6:7]
	v_lshl_add_u64 v[98:99], v[170:171], 3, s[10:11]
	global_atomic_add_x2 v[98:99], v[96:97], off
.LBB0_845:
	s_or_b64 exec, exec, s[22:23]
	s_waitcnt vmcnt(19)
	v_lshlrev_b32_e32 v98, 16, v140
	v_add_f32_e32 v92, v92, v98
	v_and_b32_e32 v98, 0xffff0000, v140
	v_add_f32_e32 v93, v93, v98
	v_lshlrev_b32_e32 v98, 16, v141
	v_add_f32_e32 v94, v94, v98
	v_and_b32_e32 v98, 0xffff0000, v141
	v_add_f32_e32 v95, v95, v98
	v_lshlrev_b32_e32 v98, 16, v142
	v_add_f32_e32 v98, v88, v98
	v_and_b32_e32 v88, 0xffff0000, v142
	v_add_f32_e32 v99, v89, v88
	v_lshlrev_b32_e32 v88, 16, v143
	v_add_f32_e32 v100, v90, v88
	v_and_b32_e32 v88, 0xffff0000, v143
	v_add_f32_e32 v101, v91, v88
	v_mul_f32_e32 v88, v93, v93
	v_mul_f32_e32 v89, v95, v95
	v_fmac_f32_e32 v88, v92, v92
	v_fmac_f32_e32 v89, v94, v94
	v_add_f32_e32 v88, v88, v89
	v_mul_f32_e32 v89, v99, v99
	v_mul_f32_e32 v90, v101, v101
	v_fmac_f32_e32 v89, v98, v98
	v_fmac_f32_e32 v90, v100, v100
	v_add_f32_e32 v89, v89, v90
	v_add_f32_e32 v102, v88, v89
	v_cvt_pk_bf16_f32 v88, v92, v93
	v_cvt_pk_bf16_f32 v89, v94, v95
	v_cvt_pk_bf16_f32 v90, v98, v99
	v_cvt_pk_bf16_f32 v91, v100, v101
	global_store_dwordx4 v[168:169], v[88:91], off
	s_waitcnt lgkmcnt(0)
	v_lshlrev_b64 v[96:97], 11, v[166:167]
	v_lshl_add_u64 v[96:97], v[96:97], 0, v[156:157]
	v_mul_f32_e32 v88, 0x41c00000, v92
	v_mul_f32_e32 v89, 0x41c00000, v93
	v_mul_f32_e32 v90, 0x41c00000, v94
	v_mul_f32_e32 v91, 0x41c00000, v95
	v_med3_f32 v88, v88, s42, v186
	v_med3_f32 v89, v89, s42, v186
	v_med3_f32 v90, v90, s42, v186
	v_med3_f32 v91, v91, s42, v186
	v_add_f32_e32 v88, 0x4b400000, v88
	v_add_f32_e32 v89, 0x4b400000, v89
	v_add_f32_e32 v90, 0x4b400000, v90
	v_add_f32_e32 v91, 0x4b400000, v91
	v_perm_b32 v88, v89, v88, s43
	v_perm_b32 v89, v91, v90, s43
	v_perm_b32 v88, v89, v88, s44
	v_mul_f32_e32 v89, 0x41c00000, v98
	v_mul_f32_e32 v90, 0x41c00000, v99
	v_mul_f32_e32 v91, 0x41c00000, v100
	v_mul_f32_e32 v92, 0x41c00000, v101
	v_med3_f32 v89, v89, s42, v186
	v_med3_f32 v90, v90, s42, v186
	v_med3_f32 v91, v91, s42, v186
	v_med3_f32 v92, v92, s42, v186
	v_add_f32_e32 v89, 0x4b400000, v89
	v_add_f32_e32 v90, 0x4b400000, v90
	v_add_f32_e32 v91, 0x4b400000, v91
	v_add_f32_e32 v92, 0x4b400000, v92
	v_perm_b32 v89, v90, v89, s43
	v_perm_b32 v90, v92, v91, s43
	v_perm_b32 v89, v90, v89, s44
	v_lshl_add_u64 v[90:91], s[14:15], 0, v[96:97]
	global_store_dwordx2 v[90:91], v[88:89], off
	s_waitcnt vmcnt(20)
	v_lshlrev_b32_e32 v88, 16, v136
	v_add_f32_e32 v84, v84, v88
	v_and_b32_e32 v88, 0xffff0000, v136
	v_add_f32_e32 v85, v85, v88
	v_lshlrev_b32_e32 v88, 16, v137
	v_add_f32_e32 v86, v86, v88
	v_and_b32_e32 v88, 0xffff0000, v137
	v_add_f32_e32 v87, v87, v88
	v_lshlrev_b32_e32 v88, 16, v138
	v_add_f32_e32 v88, v80, v88
	v_and_b32_e32 v80, 0xffff0000, v138
	v_add_f32_e32 v89, v81, v80
	v_lshlrev_b32_e32 v80, 16, v139
	v_add_f32_e32 v92, v82, v80
	v_and_b32_e32 v80, 0xffff0000, v139
	v_add_f32_e32 v93, v83, v80
	v_mul_f32_e32 v80, v85, v85
	v_mul_f32_e32 v81, v87, v87
	v_fmac_f32_e32 v80, v84, v84
	v_fmac_f32_e32 v81, v86, v86
	v_add_f32_e32 v80, v80, v81
	v_mul_f32_e32 v81, v89, v89
	v_mul_f32_e32 v82, v93, v93
	v_fmac_f32_e32 v81, v88, v88
	v_fmac_f32_e32 v82, v92, v92
	v_add_f32_e32 v81, v81, v82
	v_add_f32_e32 v80, v80, v81
	v_add_f32_e32 v94, v102, v80
	v_cvt_pk_bf16_f32 v80, v84, v85
	v_cvt_pk_bf16_f32 v81, v86, v87
	v_cvt_pk_bf16_f32 v82, v88, v89
	v_cvt_pk_bf16_f32 v83, v92, v93
	global_store_dwordx4 v[168:169], v[80:83], off offset:256
	s_nop 1
	v_mul_f32_e32 v80, 0x41c00000, v84
	v_mul_f32_e32 v81, 0x41c00000, v85
	v_mul_f32_e32 v82, 0x41c00000, v86
	v_mul_f32_e32 v83, 0x41c00000, v87
	v_med3_f32 v80, v80, s42, v186
	v_med3_f32 v81, v81, s42, v186
	v_med3_f32 v82, v82, s42, v186
	v_med3_f32 v83, v83, s42, v186
	v_add_f32_e32 v80, 0x4b400000, v80
	v_add_f32_e32 v81, 0x4b400000, v81
	v_add_f32_e32 v82, 0x4b400000, v82
	v_add_f32_e32 v83, 0x4b400000, v83
	v_perm_b32 v80, v81, v80, s43
	v_perm_b32 v81, v83, v82, s43
	v_perm_b32 v82, v81, v80, s44
	v_mul_f32_e32 v80, 0x41c00000, v88
	v_mul_f32_e32 v81, 0x41c00000, v89
	v_med3_f32 v80, v80, s42, v186
	v_add_f32_e32 v85, 0x4b400000, v80
	v_med3_f32 v80, v81, s42, v186
	v_add_f32_e32 v86, 0x4b400000, v80
	ds_bpermute_b32 v80, v179, v94
	v_mul_f32_e32 v83, 0x41c00000, v92
	v_mul_f32_e32 v84, 0x41c00000, v93
	v_med3_f32 v81, v83, s42, v186
	v_add_f32_e32 v83, 0x4b400000, v81
	v_med3_f32 v81, v84, s42, v186
	s_waitcnt lgkmcnt(0)
	v_add_f32_e32 v80, v94, v80
	v_add_f32_e32 v84, 0x4b400000, v81
	ds_bpermute_b32 v81, v180, v80
	v_perm_b32 v85, v86, v85, s43
	v_perm_b32 v83, v84, v83, s43
	v_perm_b32 v83, v83, v85, s44
	global_store_dwordx2 v[90:91], v[82:83], off offset:128
	s_and_saveexec_b64 s[22:23], vcc
	s_cbranch_execz .LBB0_847
	s_waitcnt lgkmcnt(0)
	v_add_f32_e32 v80, v80, v81
	v_mul_f32_e32 v80, 0x4b800000, v80
	v_rndne_f32_e32 v80, v80
	v_mul_f32_e64 v81, |v80|, s45
	v_floor_f32_e32 v81, v81
	v_fma_f32 v82, v81, s46, |v80|
	v_cvt_u32_f32_e32 v82, v82
	v_cvt_u32_f32_e32 v81, v81
	v_ashrrev_i32_e32 v83, 31, v80
	v_xor_b32_e32 v80, v82, v83
	v_xor_b32_e32 v81, v81, v83
	v_sub_co_u32_e64 v80, s[6:7], v80, v83
	s_nop 1
	v_subb_co_u32_e64 v81, s[6:7], v81, v83, s[6:7]
	v_lshl_add_u64 v[82:83], v[166:167], 3, s[10:11]
	global_atomic_add_x2 v[82:83], v[80:81], off
.LBB0_847:
	s_or_b64 exec, exec, s[22:23]
	s_waitcnt vmcnt(21)
	v_lshlrev_b32_e32 v82, 16, v116
	v_add_f32_e32 v76, v76, v82
	v_and_b32_e32 v82, 0xffff0000, v116
	v_add_f32_e32 v77, v77, v82
	v_lshlrev_b32_e32 v82, 16, v117
	v_add_f32_e32 v78, v78, v82
	v_and_b32_e32 v82, 0xffff0000, v117
	v_add_f32_e32 v79, v79, v82
	v_lshlrev_b32_e32 v82, 16, v118
	v_add_f32_e32 v82, v72, v82
	v_and_b32_e32 v72, 0xffff0000, v118
	v_add_f32_e32 v83, v73, v72
	v_lshlrev_b32_e32 v72, 16, v119
	v_add_f32_e32 v84, v74, v72
	v_and_b32_e32 v72, 0xffff0000, v119
	v_add_f32_e32 v85, v75, v72
	v_mul_f32_e32 v72, v77, v77
	v_mul_f32_e32 v73, v79, v79
	v_fmac_f32_e32 v72, v76, v76
	v_fmac_f32_e32 v73, v78, v78
	v_add_f32_e32 v72, v72, v73
	v_mul_f32_e32 v73, v83, v83
	v_mul_f32_e32 v74, v85, v85
	v_fmac_f32_e32 v73, v82, v82
	v_fmac_f32_e32 v74, v84, v84
	v_add_f32_e32 v73, v73, v74
	v_add_f32_e32 v86, v72, v73
	v_cvt_pk_bf16_f32 v72, v76, v77
	v_cvt_pk_bf16_f32 v73, v78, v79
	v_cvt_pk_bf16_f32 v74, v82, v83
	v_cvt_pk_bf16_f32 v75, v84, v85
	global_store_dwordx4 v[164:165], v[72:75], off
	s_waitcnt lgkmcnt(0)
	v_lshlrev_b64 v[80:81], 11, v[162:163]
	v_lshl_add_u64 v[80:81], v[80:81], 0, v[156:157]
	v_mul_f32_e32 v72, 0x41c00000, v76
	v_mul_f32_e32 v73, 0x41c00000, v77
	v_mul_f32_e32 v74, 0x41c00000, v78
	v_mul_f32_e32 v75, 0x41c00000, v79
	v_med3_f32 v72, v72, s42, v186
	v_med3_f32 v73, v73, s42, v186
	v_med3_f32 v74, v74, s42, v186
	v_med3_f32 v75, v75, s42, v186
	v_add_f32_e32 v72, 0x4b400000, v72
	v_add_f32_e32 v73, 0x4b400000, v73
	v_add_f32_e32 v74, 0x4b400000, v74
	v_add_f32_e32 v75, 0x4b400000, v75
	v_perm_b32 v72, v73, v72, s43
	v_perm_b32 v73, v75, v74, s43
	v_perm_b32 v72, v73, v72, s44
	v_mul_f32_e32 v73, 0x41c00000, v82
	v_mul_f32_e32 v74, 0x41c00000, v83
	v_mul_f32_e32 v75, 0x41c00000, v84
	v_mul_f32_e32 v76, 0x41c00000, v85
	v_med3_f32 v73, v73, s42, v186
	v_med3_f32 v74, v74, s42, v186
	v_med3_f32 v75, v75, s42, v186
	v_med3_f32 v76, v76, s42, v186
	v_add_f32_e32 v73, 0x4b400000, v73
	v_add_f32_e32 v74, 0x4b400000, v74
	v_add_f32_e32 v75, 0x4b400000, v75
	v_add_f32_e32 v76, 0x4b400000, v76
	v_perm_b32 v73, v74, v73, s43
	v_perm_b32 v74, v76, v75, s43
	v_perm_b32 v73, v74, v73, s44
	v_lshl_add_u64 v[74:75], s[14:15], 0, v[80:81]
	global_store_dwordx2 v[74:75], v[72:73], off
	s_waitcnt vmcnt(22)
	v_lshlrev_b32_e32 v72, 16, v112
	v_add_f32_e32 v68, v68, v72
	v_and_b32_e32 v72, 0xffff0000, v112
	v_add_f32_e32 v69, v69, v72
	v_lshlrev_b32_e32 v72, 16, v113
	v_add_f32_e32 v70, v70, v72
	v_and_b32_e32 v72, 0xffff0000, v113
	v_add_f32_e32 v71, v71, v72
	v_lshlrev_b32_e32 v72, 16, v114
	v_add_f32_e32 v72, v64, v72
	v_and_b32_e32 v64, 0xffff0000, v114
	v_add_f32_e32 v73, v65, v64
	v_lshlrev_b32_e32 v64, 16, v115
	v_add_f32_e32 v76, v66, v64
	v_and_b32_e32 v64, 0xffff0000, v115
	v_add_f32_e32 v77, v67, v64
	v_mul_f32_e32 v64, v69, v69
	v_mul_f32_e32 v65, v71, v71
	v_fmac_f32_e32 v64, v68, v68
	v_fmac_f32_e32 v65, v70, v70
	v_add_f32_e32 v64, v64, v65
	v_mul_f32_e32 v65, v73, v73
	v_mul_f32_e32 v66, v77, v77
	v_fmac_f32_e32 v65, v72, v72
	v_fmac_f32_e32 v66, v76, v76
	v_add_f32_e32 v65, v65, v66
	v_add_f32_e32 v64, v64, v65
	v_add_f32_e32 v78, v86, v64
	v_cvt_pk_bf16_f32 v64, v68, v69
	v_cvt_pk_bf16_f32 v65, v70, v71
	v_cvt_pk_bf16_f32 v66, v72, v73
	v_cvt_pk_bf16_f32 v67, v76, v77
	global_store_dwordx4 v[164:165], v[64:67], off offset:256
	s_nop 1
	v_mul_f32_e32 v64, 0x41c00000, v68
	v_mul_f32_e32 v65, 0x41c00000, v69
	v_mul_f32_e32 v66, 0x41c00000, v70
	v_mul_f32_e32 v67, 0x41c00000, v71
	v_med3_f32 v64, v64, s42, v186
	v_med3_f32 v65, v65, s42, v186
	v_med3_f32 v66, v66, s42, v186
	v_med3_f32 v67, v67, s42, v186
	v_add_f32_e32 v64, 0x4b400000, v64
	v_add_f32_e32 v65, 0x4b400000, v65
	v_add_f32_e32 v66, 0x4b400000, v66
	v_add_f32_e32 v67, 0x4b400000, v67
	v_perm_b32 v64, v65, v64, s43
	v_perm_b32 v65, v67, v66, s43
	v_perm_b32 v66, v65, v64, s44
	v_mul_f32_e32 v64, 0x41c00000, v72
	v_mul_f32_e32 v65, 0x41c00000, v73
	v_med3_f32 v64, v64, s42, v186
	v_add_f32_e32 v69, 0x4b400000, v64
	v_med3_f32 v64, v65, s42, v186
	v_add_f32_e32 v70, 0x4b400000, v64
	ds_bpermute_b32 v64, v179, v78
	v_mul_f32_e32 v67, 0x41c00000, v76
	v_mul_f32_e32 v68, 0x41c00000, v77
	v_med3_f32 v65, v67, s42, v186
	v_add_f32_e32 v67, 0x4b400000, v65
	v_med3_f32 v65, v68, s42, v186
	s_waitcnt lgkmcnt(0)
	v_add_f32_e32 v64, v78, v64
	v_add_f32_e32 v68, 0x4b400000, v65
	ds_bpermute_b32 v65, v180, v64
	v_perm_b32 v69, v70, v69, s43
	v_perm_b32 v67, v68, v67, s43
	v_perm_b32 v67, v67, v69, s44
	global_store_dwordx2 v[74:75], v[66:67], off offset:128
	s_and_saveexec_b64 s[22:23], vcc
	s_cbranch_execz .LBB0_849
	s_waitcnt lgkmcnt(0)
	v_add_f32_e32 v64, v64, v65
	v_mul_f32_e32 v64, 0x4b800000, v64
	v_rndne_f32_e32 v64, v64
	v_mul_f32_e64 v65, |v64|, s45
	v_floor_f32_e32 v65, v65
	v_fma_f32 v66, v65, s46, |v64|
	v_cvt_u32_f32_e32 v66, v66
	v_cvt_u32_f32_e32 v65, v65
	v_ashrrev_i32_e32 v67, 31, v64
	v_xor_b32_e32 v64, v66, v67
	v_xor_b32_e32 v65, v65, v67
	v_sub_co_u32_e64 v64, s[6:7], v64, v67
	s_nop 1
	v_subb_co_u32_e64 v65, s[6:7], v65, v67, s[6:7]
	v_lshl_add_u64 v[66:67], v[162:163], 3, s[10:11]
	global_atomic_add_x2 v[66:67], v[64:65], off
.LBB0_849:
	s_or_b64 exec, exec, s[22:23]
	v_add_u32_e32 v100, 0x80, v160
	v_ashrrev_i32_e32 v101, 31, v100
	s_waitcnt lgkmcnt(0)
	v_lshlrev_b64 v[64:65], 12, v[100:101]
	v_lshl_add_u64 v[110:111], v[158:159], 0, v[64:65]
	s_waitcnt vmcnt(16)
	v_mov_b32_e32 v102, v208
	v_mov_b32_e32 v103, v209
	v_mov_b32_e32 v104, v210
	v_mov_b32_e32 v105, v211
	v_mov_b32_e32 v106, v212
	v_mov_b32_e32 v107, v213
	v_mov_b32_e32 v108, v214
	v_mov_b32_e32 v109, v215
	v_add_u32_e32 v96, 0x90, v160
	v_add_u32_e32 v92, 0xa0, v160
	v_add_u32_e32 v88, 0xb0, v160
	v_ashrrev_i32_e32 v97, 31, v96
	v_ashrrev_i32_e32 v93, 31, v92
	v_ashrrev_i32_e32 v89, 31, v88
	v_lshlrev_b64 v[64:65], 12, v[96:97]
	v_lshlrev_b64 v[66:67], 12, v[92:93]
	v_lshlrev_b64 v[68:69], 12, v[88:89]
	v_lshlrev_b64 v[70:71], 11, v[100:101]
	v_lshl_add_u64 v[98:99], v[158:159], 0, v[64:65]
	v_lshl_add_u64 v[94:95], v[158:159], 0, v[66:67]
	v_lshl_add_u64 v[90:91], v[158:159], 0, v[68:69]
	v_lshl_add_u64 v[112:113], v[70:71], 0, v[156:157]
	v_mov_b32_e32 v84, v216
	v_mov_b32_e32 v85, v217
	v_mov_b32_e32 v86, v218
	v_mov_b32_e32 v87, v219
	v_mov_b32_e32 v80, v220
	v_mov_b32_e32 v81, v221
	v_mov_b32_e32 v82, v222
	v_mov_b32_e32 v83, v223
	v_mov_b32_e32 v76, v224
	v_mov_b32_e32 v77, v225
	v_mov_b32_e32 v78, v226
	v_mov_b32_e32 v79, v227
	v_mov_b32_e32 v72, v228
	v_mov_b32_e32 v73, v229
	v_mov_b32_e32 v74, v230
	v_mov_b32_e32 v75, v231
	v_mov_b32_e32 v68, v232
	v_mov_b32_e32 v69, v233
	v_mov_b32_e32 v70, v234
	v_mov_b32_e32 v71, v235
	v_mov_b32_e32 v64, v236
	v_mov_b32_e32 v65, v237
	v_mov_b32_e32 v66, v238
	v_mov_b32_e32 v67, v239
	v_lshl_add_u64 v[112:113], s[14:15], 0, v[112:113]
	v_lshlrev_b32_e32 v114, 16, v102
	v_and_b32_e32 v102, 0xffff0000, v102
	v_lshlrev_b32_e32 v115, 16, v103
	v_and_b32_e32 v103, 0xffff0000, v103
	v_lshlrev_b32_e32 v116, 16, v104
	v_and_b32_e32 v104, 0xffff0000, v104
	v_lshlrev_b32_e32 v117, 16, v105
	v_and_b32_e32 v105, 0xffff0000, v105
	v_add_f32_e32 v60, v60, v114
	v_add_f32_e32 v61, v61, v102
	v_add_f32_e32 v62, v62, v115
	v_add_f32_e32 v63, v63, v103
	v_add_f32_e32 v102, v56, v116
	v_add_f32_e32 v103, v57, v104
	v_add_f32_e32 v104, v58, v117
	v_add_f32_e32 v105, v59, v105
	v_mul_f32_e32 v114, v61, v61
	v_mul_f32_e32 v115, v63, v63
	v_mul_f32_e32 v116, v103, v103
	v_mul_f32_e32 v117, v105, v105
	v_cvt_pk_bf16_f32 v56, v60, v61
	v_cvt_pk_bf16_f32 v57, v62, v63
	v_cvt_pk_bf16_f32 v58, v102, v103
	v_cvt_pk_bf16_f32 v59, v104, v105
	v_mul_f32_e32 v119, 0x41c00000, v60
	v_mul_f32_e32 v61, 0x41c00000, v61
	v_mul_f32_e32 v120, 0x41c00000, v62
	v_mul_f32_e32 v63, 0x41c00000, v63
	v_mul_f32_e32 v121, 0x41c00000, v102
	v_mul_f32_e32 v103, 0x41c00000, v103
	v_mul_f32_e32 v122, 0x41c00000, v104
	v_mul_f32_e32 v105, 0x41c00000, v105
	v_fmac_f32_e32 v114, v60, v60
	v_fmac_f32_e32 v115, v62, v62
	global_store_dwordx4 v[110:111], v[56:59], off
	v_med3_f32 v60, v121, s42, v186
	v_med3_f32 v62, v122, s42, v186
	v_med3_f32 v56, v119, s42, v186
	v_med3_f32 v57, v61, s42, v186
	v_med3_f32 v58, v120, s42, v186
	v_med3_f32 v59, v63, s42, v186
	v_med3_f32 v61, v103, s42, v186
	v_med3_f32 v63, v105, s42, v186
	v_add_f32_e32 v56, 0x4b400000, v56
	v_add_f32_e32 v57, 0x4b400000, v57
	v_add_f32_e32 v58, 0x4b400000, v58
	v_add_f32_e32 v59, 0x4b400000, v59
	v_add_f32_e32 v60, 0x4b400000, v60
	v_add_f32_e32 v61, 0x4b400000, v61
	v_add_f32_e32 v62, 0x4b400000, v62
	v_add_f32_e32 v63, 0x4b400000, v63
	v_perm_b32 v56, v57, v56, s43
	v_perm_b32 v57, v59, v58, s43
	v_perm_b32 v58, v61, v60, s43
	v_perm_b32 v59, v63, v62, s43
	v_perm_b32 v56, v57, v56, s44
	v_perm_b32 v57, v59, v58, s44
	global_store_dwordx2 v[112:113], v[56:57], off
	v_and_b32_e32 v56, 0xffff0000, v106
	v_add_f32_e32 v53, v53, v56
	v_lshlrev_b32_e32 v56, 16, v107
	v_add_f32_e32 v54, v54, v56
	v_and_b32_e32 v56, 0xffff0000, v107
	v_add_f32_e32 v55, v55, v56
	v_lshlrev_b32_e32 v56, 16, v108
	v_add_f32_e32 v56, v48, v56
	v_and_b32_e32 v48, 0xffff0000, v108
	v_add_f32_e32 v57, v49, v48
	v_lshlrev_b32_e32 v48, 16, v109
	v_lshlrev_b32_e32 v118, 16, v106
	v_add_f32_e32 v58, v50, v48
	v_and_b32_e32 v48, 0xffff0000, v109
	v_add_f32_e32 v52, v52, v118
	v_add_f32_e32 v59, v51, v48
	v_mul_f32_e32 v48, v53, v53
	v_mul_f32_e32 v49, v55, v55
	v_fmac_f32_e32 v48, v52, v52
	v_fmac_f32_e32 v49, v54, v54
	v_add_f32_e32 v48, v48, v49
	v_mul_f32_e32 v49, v57, v57
	v_mul_f32_e32 v50, v59, v59
	v_fmac_f32_e32 v116, v102, v102
	v_fmac_f32_e32 v117, v104, v104
	v_fmac_f32_e32 v49, v56, v56
	v_fmac_f32_e32 v50, v58, v58
	v_add_f32_e32 v102, v114, v115
	v_add_f32_e32 v103, v116, v117
	v_add_f32_e32 v49, v49, v50
	v_add_f32_e32 v102, v102, v103
	v_add_f32_e32 v48, v48, v49
	v_add_f32_e32 v60, v102, v48
	v_cvt_pk_bf16_f32 v48, v52, v53
	v_cvt_pk_bf16_f32 v49, v54, v55
	v_cvt_pk_bf16_f32 v50, v56, v57
	v_cvt_pk_bf16_f32 v51, v58, v59
	global_store_dwordx4 v[110:111], v[48:51], off offset:256
	s_nop 1
	v_mul_f32_e32 v48, 0x41c00000, v52
	v_mul_f32_e32 v49, 0x41c00000, v53
	v_mul_f32_e32 v50, 0x41c00000, v54
	v_mul_f32_e32 v51, 0x41c00000, v55
	v_med3_f32 v48, v48, s42, v186
	v_med3_f32 v49, v49, s42, v186
	v_med3_f32 v50, v50, s42, v186
	v_med3_f32 v51, v51, s42, v186
	v_add_f32_e32 v48, 0x4b400000, v48
	v_add_f32_e32 v49, 0x4b400000, v49
	v_add_f32_e32 v50, 0x4b400000, v50
	v_add_f32_e32 v51, 0x4b400000, v51
	v_perm_b32 v48, v49, v48, s43
	v_perm_b32 v49, v51, v50, s43
	v_perm_b32 v50, v49, v48, s44
	v_mul_f32_e32 v48, 0x41c00000, v56
	v_mul_f32_e32 v49, 0x41c00000, v57
	v_med3_f32 v48, v48, s42, v186
	v_add_f32_e32 v53, 0x4b400000, v48
	v_med3_f32 v48, v49, s42, v186
	v_add_f32_e32 v54, 0x4b400000, v48
	ds_bpermute_b32 v48, v179, v60
	v_mul_f32_e32 v51, 0x41c00000, v58
	v_mul_f32_e32 v52, 0x41c00000, v59
	v_med3_f32 v49, v51, s42, v186
	v_add_f32_e32 v51, 0x4b400000, v49
	v_med3_f32 v49, v52, s42, v186
	s_waitcnt lgkmcnt(0)
	v_add_f32_e32 v48, v60, v48
	v_add_f32_e32 v52, 0x4b400000, v49
	ds_bpermute_b32 v49, v180, v48
	v_perm_b32 v53, v54, v53, s43
	v_perm_b32 v51, v52, v51, s43
	v_perm_b32 v51, v51, v53, s44
	global_store_dwordx2 v[112:113], v[50:51], off offset:128
	s_and_saveexec_b64 s[22:23], vcc
	s_cbranch_execz .LBB0_851
	s_waitcnt lgkmcnt(0)
	v_add_f32_e32 v48, v48, v49
	v_mul_f32_e32 v48, 0x4b800000, v48
	v_rndne_f32_e32 v48, v48
	v_mul_f32_e64 v49, |v48|, s45
	v_floor_f32_e32 v49, v49
	v_fma_f32 v50, v49, s46, |v48|
	v_cvt_u32_f32_e32 v50, v50
	v_cvt_u32_f32_e32 v49, v49
	v_ashrrev_i32_e32 v51, 31, v48
	v_xor_b32_e32 v48, v50, v51
	v_xor_b32_e32 v49, v49, v51
	v_sub_co_u32_e64 v48, s[6:7], v48, v51
	s_nop 1
	v_subb_co_u32_e64 v49, s[6:7], v49, v51, s[6:7]
	v_lshl_add_u64 v[50:51], v[100:101], 3, s[10:11]
	global_atomic_add_x2 v[50:51], v[48:49], off
.LBB0_851:
	s_or_b64 exec, exec, s[22:23]
	v_lshlrev_b32_e32 v50, 16, v84
	v_add_f32_e32 v44, v44, v50
	v_and_b32_e32 v50, 0xffff0000, v84
	v_add_f32_e32 v45, v45, v50
	v_lshlrev_b32_e32 v50, 16, v85
	v_add_f32_e32 v46, v46, v50
	v_and_b32_e32 v50, 0xffff0000, v85
	v_add_f32_e32 v47, v47, v50
	v_lshlrev_b32_e32 v50, 16, v86
	v_add_f32_e32 v50, v40, v50
	v_and_b32_e32 v40, 0xffff0000, v86
	v_add_f32_e32 v51, v41, v40
	v_lshlrev_b32_e32 v40, 16, v87
	v_add_f32_e32 v52, v42, v40
	v_and_b32_e32 v40, 0xffff0000, v87
	v_add_f32_e32 v53, v43, v40
	v_mul_f32_e32 v40, v45, v45
	v_mul_f32_e32 v41, v47, v47
	v_fmac_f32_e32 v40, v44, v44
	v_fmac_f32_e32 v41, v46, v46
	v_add_f32_e32 v40, v40, v41
	v_mul_f32_e32 v41, v51, v51
	v_mul_f32_e32 v42, v53, v53
	v_fmac_f32_e32 v41, v50, v50
	v_fmac_f32_e32 v42, v52, v52
	v_add_f32_e32 v41, v41, v42
	v_add_f32_e32 v54, v40, v41
	v_cvt_pk_bf16_f32 v40, v44, v45
	v_cvt_pk_bf16_f32 v41, v46, v47
	v_cvt_pk_bf16_f32 v42, v50, v51
	v_cvt_pk_bf16_f32 v43, v52, v53
	global_store_dwordx4 v[98:99], v[40:43], off
	s_waitcnt lgkmcnt(0)
	v_lshlrev_b64 v[48:49], 11, v[96:97]
	v_lshl_add_u64 v[48:49], v[48:49], 0, v[156:157]
	v_mul_f32_e32 v40, 0x41c00000, v44
	v_mul_f32_e32 v41, 0x41c00000, v45
	v_mul_f32_e32 v42, 0x41c00000, v46
	v_mul_f32_e32 v43, 0x41c00000, v47
	v_med3_f32 v40, v40, s42, v186
	v_med3_f32 v41, v41, s42, v186
	v_med3_f32 v42, v42, s42, v186
	v_med3_f32 v43, v43, s42, v186
	v_add_f32_e32 v40, 0x4b400000, v40
	v_add_f32_e32 v41, 0x4b400000, v41
	v_add_f32_e32 v42, 0x4b400000, v42
	v_add_f32_e32 v43, 0x4b400000, v43
	v_perm_b32 v40, v41, v40, s43
	v_perm_b32 v41, v43, v42, s43
	v_perm_b32 v40, v41, v40, s44
	v_mul_f32_e32 v41, 0x41c00000, v50
	v_mul_f32_e32 v42, 0x41c00000, v51
	v_mul_f32_e32 v43, 0x41c00000, v52
	v_mul_f32_e32 v44, 0x41c00000, v53
	v_med3_f32 v41, v41, s42, v186
	v_med3_f32 v42, v42, s42, v186
	v_med3_f32 v43, v43, s42, v186
	v_med3_f32 v44, v44, s42, v186
	v_add_f32_e32 v41, 0x4b400000, v41
	v_add_f32_e32 v42, 0x4b400000, v42
	v_add_f32_e32 v43, 0x4b400000, v43
	v_add_f32_e32 v44, 0x4b400000, v44
	v_perm_b32 v41, v42, v41, s43
	v_perm_b32 v42, v44, v43, s43
	v_perm_b32 v41, v42, v41, s44
	v_lshl_add_u64 v[42:43], s[14:15], 0, v[48:49]
	global_store_dwordx2 v[42:43], v[40:41], off
	v_lshlrev_b32_e32 v40, 16, v80
	v_add_f32_e32 v36, v36, v40
	v_and_b32_e32 v40, 0xffff0000, v80
	v_add_f32_e32 v37, v37, v40
	v_lshlrev_b32_e32 v40, 16, v81
	v_add_f32_e32 v38, v38, v40
	v_and_b32_e32 v40, 0xffff0000, v81
	v_add_f32_e32 v39, v39, v40
	v_lshlrev_b32_e32 v40, 16, v82
	v_add_f32_e32 v40, v32, v40
	v_and_b32_e32 v32, 0xffff0000, v82
	v_add_f32_e32 v41, v33, v32
	v_lshlrev_b32_e32 v32, 16, v83
	v_add_f32_e32 v44, v34, v32
	v_and_b32_e32 v32, 0xffff0000, v83
	v_add_f32_e32 v45, v35, v32
	v_mul_f32_e32 v32, v37, v37
	v_mul_f32_e32 v33, v39, v39
	v_fmac_f32_e32 v32, v36, v36
	v_fmac_f32_e32 v33, v38, v38
	v_add_f32_e32 v32, v32, v33
	v_mul_f32_e32 v33, v41, v41
	v_mul_f32_e32 v34, v45, v45
	v_fmac_f32_e32 v33, v40, v40
	v_fmac_f32_e32 v34, v44, v44
	v_add_f32_e32 v33, v33, v34
	v_add_f32_e32 v32, v32, v33
	v_add_f32_e32 v46, v54, v32
	v_cvt_pk_bf16_f32 v32, v36, v37
	v_cvt_pk_bf16_f32 v33, v38, v39
	v_cvt_pk_bf16_f32 v34, v40, v41
	v_cvt_pk_bf16_f32 v35, v44, v45
	global_store_dwordx4 v[98:99], v[32:35], off offset:256
	s_nop 1
	v_mul_f32_e32 v32, 0x41c00000, v36
	v_mul_f32_e32 v33, 0x41c00000, v37
	v_mul_f32_e32 v34, 0x41c00000, v38
	v_mul_f32_e32 v35, 0x41c00000, v39
	v_med3_f32 v32, v32, s42, v186
	v_med3_f32 v33, v33, s42, v186
	v_med3_f32 v34, v34, s42, v186
	v_med3_f32 v35, v35, s42, v186
	v_add_f32_e32 v32, 0x4b400000, v32
	v_add_f32_e32 v33, 0x4b400000, v33
	v_add_f32_e32 v34, 0x4b400000, v34
	v_add_f32_e32 v35, 0x4b400000, v35
	v_perm_b32 v32, v33, v32, s43
	v_perm_b32 v33, v35, v34, s43
	v_perm_b32 v34, v33, v32, s44
	v_mul_f32_e32 v32, 0x41c00000, v40
	v_mul_f32_e32 v33, 0x41c00000, v41
	v_med3_f32 v32, v32, s42, v186
	v_add_f32_e32 v37, 0x4b400000, v32
	v_med3_f32 v32, v33, s42, v186
	v_add_f32_e32 v38, 0x4b400000, v32
	ds_bpermute_b32 v32, v179, v46
	v_mul_f32_e32 v35, 0x41c00000, v44
	v_mul_f32_e32 v36, 0x41c00000, v45
	v_med3_f32 v33, v35, s42, v186
	v_add_f32_e32 v35, 0x4b400000, v33
	v_med3_f32 v33, v36, s42, v186
	s_waitcnt lgkmcnt(0)
	v_add_f32_e32 v32, v46, v32
	v_add_f32_e32 v36, 0x4b400000, v33
	ds_bpermute_b32 v33, v180, v32
	v_perm_b32 v37, v38, v37, s43
	v_perm_b32 v35, v36, v35, s43
	v_perm_b32 v35, v35, v37, s44
	global_store_dwordx2 v[42:43], v[34:35], off offset:128
	s_and_saveexec_b64 s[22:23], vcc
	s_cbranch_execz .LBB0_853
	s_waitcnt lgkmcnt(0)
	v_add_f32_e32 v32, v32, v33
	v_mul_f32_e32 v32, 0x4b800000, v32
	v_rndne_f32_e32 v32, v32
	v_mul_f32_e64 v33, |v32|, s45
	v_floor_f32_e32 v33, v33
	v_fma_f32 v34, v33, s46, |v32|
	v_cvt_u32_f32_e32 v34, v34
	v_cvt_u32_f32_e32 v33, v33
	v_ashrrev_i32_e32 v35, 31, v32
	v_xor_b32_e32 v32, v34, v35
	v_xor_b32_e32 v33, v33, v35
	v_sub_co_u32_e64 v32, s[6:7], v32, v35
	s_nop 1
	v_subb_co_u32_e64 v33, s[6:7], v33, v35, s[6:7]
	v_lshl_add_u64 v[34:35], v[96:97], 3, s[10:11]
	global_atomic_add_x2 v[34:35], v[32:33], off
.LBB0_853:
	s_or_b64 exec, exec, s[22:23]
	v_lshlrev_b32_e32 v34, 16, v76
	v_add_f32_e32 v28, v28, v34
	v_and_b32_e32 v34, 0xffff0000, v76
	v_add_f32_e32 v29, v29, v34
	v_lshlrev_b32_e32 v34, 16, v77
	v_add_f32_e32 v30, v30, v34
	v_and_b32_e32 v34, 0xffff0000, v77
	v_add_f32_e32 v31, v31, v34
	v_lshlrev_b32_e32 v34, 16, v78
	v_add_f32_e32 v34, v24, v34
	v_and_b32_e32 v24, 0xffff0000, v78
	v_add_f32_e32 v35, v25, v24
	v_lshlrev_b32_e32 v24, 16, v79
	v_add_f32_e32 v36, v26, v24
	v_and_b32_e32 v24, 0xffff0000, v79
	v_add_f32_e32 v37, v27, v24
	v_mul_f32_e32 v24, v29, v29
	v_mul_f32_e32 v25, v31, v31
	v_fmac_f32_e32 v24, v28, v28
	v_fmac_f32_e32 v25, v30, v30
	v_add_f32_e32 v24, v24, v25
	v_mul_f32_e32 v25, v35, v35
	v_mul_f32_e32 v26, v37, v37
	v_fmac_f32_e32 v25, v34, v34
	v_fmac_f32_e32 v26, v36, v36
	v_add_f32_e32 v25, v25, v26
	v_add_f32_e32 v38, v24, v25
	v_cvt_pk_bf16_f32 v24, v28, v29
	v_cvt_pk_bf16_f32 v25, v30, v31
	v_cvt_pk_bf16_f32 v26, v34, v35
	v_cvt_pk_bf16_f32 v27, v36, v37
	global_store_dwordx4 v[94:95], v[24:27], off
	s_waitcnt lgkmcnt(0)
	v_lshlrev_b64 v[32:33], 11, v[92:93]
	v_lshl_add_u64 v[32:33], v[32:33], 0, v[156:157]
	v_mul_f32_e32 v24, 0x41c00000, v28
	v_mul_f32_e32 v25, 0x41c00000, v29
	v_mul_f32_e32 v26, 0x41c00000, v30
	v_mul_f32_e32 v27, 0x41c00000, v31
	v_med3_f32 v24, v24, s42, v186
	v_med3_f32 v25, v25, s42, v186
	v_med3_f32 v26, v26, s42, v186
	v_med3_f32 v27, v27, s42, v186
	v_add_f32_e32 v24, 0x4b400000, v24
	v_add_f32_e32 v25, 0x4b400000, v25
	v_add_f32_e32 v26, 0x4b400000, v26
	v_add_f32_e32 v27, 0x4b400000, v27
	v_perm_b32 v24, v25, v24, s43
	v_perm_b32 v25, v27, v26, s43
	v_perm_b32 v24, v25, v24, s44
	v_mul_f32_e32 v25, 0x41c00000, v34
	v_mul_f32_e32 v26, 0x41c00000, v35
	v_mul_f32_e32 v27, 0x41c00000, v36
	v_mul_f32_e32 v28, 0x41c00000, v37
	v_med3_f32 v25, v25, s42, v186
	v_med3_f32 v26, v26, s42, v186
	v_med3_f32 v27, v27, s42, v186
	v_med3_f32 v28, v28, s42, v186
	v_add_f32_e32 v25, 0x4b400000, v25
	v_add_f32_e32 v26, 0x4b400000, v26
	v_add_f32_e32 v27, 0x4b400000, v27
	v_add_f32_e32 v28, 0x4b400000, v28
	v_perm_b32 v25, v26, v25, s43
	v_perm_b32 v26, v28, v27, s43
	v_perm_b32 v25, v26, v25, s44
	v_lshl_add_u64 v[26:27], s[14:15], 0, v[32:33]
	global_store_dwordx2 v[26:27], v[24:25], off
	v_lshlrev_b32_e32 v24, 16, v72
	v_add_f32_e32 v20, v20, v24
	v_and_b32_e32 v24, 0xffff0000, v72
	v_add_f32_e32 v21, v21, v24
	v_lshlrev_b32_e32 v24, 16, v73
	v_add_f32_e32 v22, v22, v24
	v_and_b32_e32 v24, 0xffff0000, v73
	v_add_f32_e32 v23, v23, v24
	v_lshlrev_b32_e32 v24, 16, v74
	v_add_f32_e32 v24, v16, v24
	v_and_b32_e32 v16, 0xffff0000, v74
	v_add_f32_e32 v25, v17, v16
	v_lshlrev_b32_e32 v16, 16, v75
	v_add_f32_e32 v28, v18, v16
	v_and_b32_e32 v16, 0xffff0000, v75
	v_add_f32_e32 v29, v19, v16
	v_mul_f32_e32 v16, v21, v21
	v_mul_f32_e32 v17, v23, v23
	v_fmac_f32_e32 v16, v20, v20
	v_fmac_f32_e32 v17, v22, v22
	v_add_f32_e32 v16, v16, v17
	v_mul_f32_e32 v17, v25, v25
	v_mul_f32_e32 v18, v29, v29
	v_fmac_f32_e32 v17, v24, v24
	v_fmac_f32_e32 v18, v28, v28
	v_add_f32_e32 v17, v17, v18
	v_add_f32_e32 v16, v16, v17
	v_add_f32_e32 v30, v38, v16
	v_cvt_pk_bf16_f32 v16, v20, v21
	v_cvt_pk_bf16_f32 v17, v22, v23
	v_cvt_pk_bf16_f32 v18, v24, v25
	v_cvt_pk_bf16_f32 v19, v28, v29
	global_store_dwordx4 v[94:95], v[16:19], off offset:256
	s_nop 1
	v_mul_f32_e32 v16, 0x41c00000, v20
	v_mul_f32_e32 v17, 0x41c00000, v21
	v_mul_f32_e32 v18, 0x41c00000, v22
	v_mul_f32_e32 v19, 0x41c00000, v23
	v_med3_f32 v16, v16, s42, v186
	v_med3_f32 v17, v17, s42, v186
	v_med3_f32 v18, v18, s42, v186
	v_med3_f32 v19, v19, s42, v186
	v_add_f32_e32 v16, 0x4b400000, v16
	v_add_f32_e32 v17, 0x4b400000, v17
	v_add_f32_e32 v18, 0x4b400000, v18
	v_add_f32_e32 v19, 0x4b400000, v19
	v_perm_b32 v16, v17, v16, s43
	v_perm_b32 v17, v19, v18, s43
	v_perm_b32 v18, v17, v16, s44
	v_mul_f32_e32 v16, 0x41c00000, v24
	v_mul_f32_e32 v17, 0x41c00000, v25
	v_med3_f32 v16, v16, s42, v186
	v_add_f32_e32 v21, 0x4b400000, v16
	v_med3_f32 v16, v17, s42, v186
	v_add_f32_e32 v22, 0x4b400000, v16
	ds_bpermute_b32 v16, v179, v30
	v_mul_f32_e32 v19, 0x41c00000, v28
	v_mul_f32_e32 v20, 0x41c00000, v29
	v_med3_f32 v17, v19, s42, v186
	v_add_f32_e32 v19, 0x4b400000, v17
	v_med3_f32 v17, v20, s42, v186
	s_waitcnt lgkmcnt(0)
	v_add_f32_e32 v16, v30, v16
	v_add_f32_e32 v20, 0x4b400000, v17
	ds_bpermute_b32 v17, v180, v16
	v_perm_b32 v21, v22, v21, s43
	v_perm_b32 v19, v20, v19, s43
	v_perm_b32 v19, v19, v21, s44
	global_store_dwordx2 v[26:27], v[18:19], off offset:128
	s_and_saveexec_b64 s[22:23], vcc
	s_cbranch_execz .LBB0_855
	s_waitcnt lgkmcnt(0)
	v_add_f32_e32 v16, v16, v17
	v_mul_f32_e32 v16, 0x4b800000, v16
	v_rndne_f32_e32 v16, v16
	v_mul_f32_e64 v17, |v16|, s45
	v_floor_f32_e32 v17, v17
	v_fma_f32 v18, v17, s46, |v16|
	v_cvt_u32_f32_e32 v18, v18
	v_cvt_u32_f32_e32 v17, v17
	v_ashrrev_i32_e32 v19, 31, v16
	v_xor_b32_e32 v16, v18, v19
	v_xor_b32_e32 v17, v17, v19
	v_sub_co_u32_e64 v16, s[6:7], v16, v19
	s_nop 1
	v_subb_co_u32_e64 v17, s[6:7], v17, v19, s[6:7]
	v_lshl_add_u64 v[18:19], v[92:93], 3, s[10:11]
	global_atomic_add_x2 v[18:19], v[16:17], off
.LBB0_855:
	s_or_b64 exec, exec, s[22:23]
	v_lshlrev_b32_e32 v18, 16, v68
	v_add_f32_e32 v12, v12, v18
	v_and_b32_e32 v18, 0xffff0000, v68
	v_add_f32_e32 v13, v13, v18
	v_lshlrev_b32_e32 v18, 16, v69
	v_add_f32_e32 v14, v14, v18
	v_and_b32_e32 v18, 0xffff0000, v69
	v_add_f32_e32 v15, v15, v18
	v_lshlrev_b32_e32 v18, 16, v70
	v_add_f32_e32 v18, v8, v18
	v_and_b32_e32 v8, 0xffff0000, v70
	v_add_f32_e32 v19, v9, v8
	v_lshlrev_b32_e32 v8, 16, v71
	v_add_f32_e32 v20, v10, v8
	v_and_b32_e32 v8, 0xffff0000, v71
	v_add_f32_e32 v21, v11, v8
	v_mul_f32_e32 v8, v13, v13
	v_mul_f32_e32 v9, v15, v15
	v_fmac_f32_e32 v8, v12, v12
	v_fmac_f32_e32 v9, v14, v14
	v_add_f32_e32 v8, v8, v9
	v_mul_f32_e32 v9, v19, v19
	v_mul_f32_e32 v10, v21, v21
	v_fmac_f32_e32 v9, v18, v18
	v_fmac_f32_e32 v10, v20, v20
	v_add_f32_e32 v9, v9, v10
	v_add_f32_e32 v22, v8, v9
	v_cvt_pk_bf16_f32 v8, v12, v13
	v_cvt_pk_bf16_f32 v9, v14, v15
	v_cvt_pk_bf16_f32 v10, v18, v19
	v_cvt_pk_bf16_f32 v11, v20, v21
	global_store_dwordx4 v[90:91], v[8:11], off
	s_waitcnt lgkmcnt(0)
	v_lshlrev_b64 v[16:17], 11, v[88:89]
	v_lshl_add_u64 v[16:17], v[16:17], 0, v[156:157]
	v_mul_f32_e32 v8, 0x41c00000, v12
	v_mul_f32_e32 v9, 0x41c00000, v13
	v_mul_f32_e32 v10, 0x41c00000, v14
	v_mul_f32_e32 v11, 0x41c00000, v15
	v_med3_f32 v8, v8, s42, v186
	v_med3_f32 v9, v9, s42, v186
	v_med3_f32 v10, v10, s42, v186
	v_med3_f32 v11, v11, s42, v186
	v_add_f32_e32 v8, 0x4b400000, v8
	v_add_f32_e32 v9, 0x4b400000, v9
	v_add_f32_e32 v10, 0x4b400000, v10
	v_add_f32_e32 v11, 0x4b400000, v11
	v_perm_b32 v8, v9, v8, s43
	v_perm_b32 v9, v11, v10, s43
	v_perm_b32 v8, v9, v8, s44
	v_mul_f32_e32 v9, 0x41c00000, v18
	v_mul_f32_e32 v10, 0x41c00000, v19
	v_mul_f32_e32 v11, 0x41c00000, v20
	v_mul_f32_e32 v12, 0x41c00000, v21
	v_med3_f32 v9, v9, s42, v186
	v_med3_f32 v10, v10, s42, v186
	v_med3_f32 v11, v11, s42, v186
	v_med3_f32 v12, v12, s42, v186
	v_add_f32_e32 v9, 0x4b400000, v9
	v_add_f32_e32 v10, 0x4b400000, v10
	v_add_f32_e32 v11, 0x4b400000, v11
	v_add_f32_e32 v12, 0x4b400000, v12
	v_perm_b32 v9, v10, v9, s43
	v_perm_b32 v10, v12, v11, s43
	v_perm_b32 v9, v10, v9, s44
	v_lshl_add_u64 v[10:11], s[14:15], 0, v[16:17]
	global_store_dwordx2 v[10:11], v[8:9], off
	v_lshlrev_b32_e32 v8, 16, v64
	v_add_f32_e32 v4, v4, v8
	v_and_b32_e32 v8, 0xffff0000, v64
	v_add_f32_e32 v5, v5, v8
	v_lshlrev_b32_e32 v8, 16, v65
	v_add_f32_e32 v6, v6, v8
	v_and_b32_e32 v8, 0xffff0000, v65
	v_add_f32_e32 v7, v7, v8
	v_lshlrev_b32_e32 v8, 16, v66
	v_add_f32_e32 v8, v0, v8
	v_and_b32_e32 v0, 0xffff0000, v66
	v_add_f32_e32 v9, v1, v0
	v_lshlrev_b32_e32 v0, 16, v67
	v_add_f32_e32 v12, v2, v0
	v_and_b32_e32 v0, 0xffff0000, v67
	v_add_f32_e32 v13, v3, v0
	v_mul_f32_e32 v0, v5, v5
	v_mul_f32_e32 v1, v7, v7
	v_fmac_f32_e32 v0, v4, v4
	v_fmac_f32_e32 v1, v6, v6
	v_add_f32_e32 v0, v0, v1
	v_mul_f32_e32 v1, v9, v9
	v_mul_f32_e32 v2, v13, v13
	v_fmac_f32_e32 v1, v8, v8
	v_fmac_f32_e32 v2, v12, v12
	v_add_f32_e32 v1, v1, v2
	v_add_f32_e32 v0, v0, v1
	v_add_f32_e32 v14, v22, v0
	v_cvt_pk_bf16_f32 v0, v4, v5
	v_cvt_pk_bf16_f32 v1, v6, v7
	v_cvt_pk_bf16_f32 v2, v8, v9
	v_cvt_pk_bf16_f32 v3, v12, v13
	global_store_dwordx4 v[90:91], v[0:3], off offset:256
	s_nop 1
	v_mul_f32_e32 v0, 0x41c00000, v4
	v_mul_f32_e32 v1, 0x41c00000, v5
	v_mul_f32_e32 v2, 0x41c00000, v6
	v_mul_f32_e32 v3, 0x41c00000, v7
	v_med3_f32 v0, v0, s42, v186
	v_med3_f32 v1, v1, s42, v186
	v_med3_f32 v2, v2, s42, v186
	v_med3_f32 v3, v3, s42, v186
	v_add_f32_e32 v0, 0x4b400000, v0
	v_add_f32_e32 v1, 0x4b400000, v1
	v_add_f32_e32 v2, 0x4b400000, v2
	v_add_f32_e32 v3, 0x4b400000, v3
	v_perm_b32 v0, v1, v0, s43
	v_perm_b32 v1, v3, v2, s43
	v_perm_b32 v2, v1, v0, s44
	v_mul_f32_e32 v0, 0x41c00000, v8
	v_mul_f32_e32 v1, 0x41c00000, v9
	v_med3_f32 v0, v0, s42, v186
	v_add_f32_e32 v5, 0x4b400000, v0
	v_med3_f32 v0, v1, s42, v186
	v_add_f32_e32 v6, 0x4b400000, v0
	ds_bpermute_b32 v0, v179, v14
	v_mul_f32_e32 v3, 0x41c00000, v12
	v_mul_f32_e32 v4, 0x41c00000, v13
	v_med3_f32 v1, v3, s42, v186
	v_add_f32_e32 v3, 0x4b400000, v1
	v_med3_f32 v1, v4, s42, v186
	s_waitcnt lgkmcnt(0)
	v_add_f32_e32 v0, v14, v0
	v_add_f32_e32 v4, 0x4b400000, v1
	ds_bpermute_b32 v1, v180, v0
	v_perm_b32 v5, v6, v5, s43
	v_perm_b32 v3, v4, v3, s43
	v_perm_b32 v3, v3, v5, s44
	global_store_dwordx2 v[10:11], v[2:3], off offset:128
	s_and_saveexec_b64 s[6:7], vcc
	s_cbranch_execz .LBB0_857
	s_waitcnt lgkmcnt(0)
	v_add_f32_e32 v0, v0, v1
	v_mul_f32_e32 v0, 0x4b800000, v0
	v_rndne_f32_e32 v0, v0
	v_mul_f32_e64 v1, |v0|, s45
	v_floor_f32_e32 v1, v1
	v_fma_f32 v2, v1, s46, |v0|
	v_cvt_u32_f32_e32 v2, v2
	v_cvt_u32_f32_e32 v1, v1
	v_ashrrev_i32_e32 v3, 31, v0
	v_xor_b32_e32 v0, v2, v3
	v_xor_b32_e32 v1, v1, v3
	v_sub_co_u32_e32 v0, vcc, v0, v3
	s_nop 1
	v_subb_co_u32_e32 v1, vcc, v1, v3, vcc
	v_lshl_add_u64 v[2:3], v[88:89], 3, s[10:11]
	global_atomic_add_x2 v[2:3], v[0:1], off

.LBB0_1112:
	v_mov_b32_e32 v132, v138
	s_lshl_b32 s21, s28, 8
	s_add_i32 s21, s21, s47
	v_and_or_b32 v164, v132, 15, s21
	s_lshl_b32 s21, s50, 8
	v_ashrrev_i32_e32 v132, 1, v132
	s_or_b32 s21, s21, s48
	v_and_b32_e32 v132, -8, v132
	v_add_u32_e32 v132, s21, v132
	v_ashrrev_i32_e32 v133, 31, v132
	v_or_b32_e32 v156, 16, v164
	v_lshlrev_b64 v[132:133], 1, v[132:133]
	v_ashrrev_i32_e32 v165, 31, v164
	v_ashrrev_i32_e32 v157, 31, v156
	v_lshl_add_u64 v[134:135], s[12:13], 0, v[132:133]
	v_lshlrev_b64 v[136:137], 12, v[164:165]
	v_lshlrev_b64 v[180:181], 12, v[156:157]
	v_lshl_add_u64 v[152:153], v[134:135], 0, v[136:137]
	v_lshl_add_u64 v[160:161], v[134:135], 0, v[180:181]
	global_load_dwordx4 v[148:151], v[152:153], off
	s_nop 0
	global_load_dwordx4 v[152:155], v[152:153], off offset:256
	s_nop 0
	global_load_dwordx4 v[156:159], v[160:161], off
	s_nop 0
	global_load_dwordx4 v[160:163], v[160:161], off offset:256
	v_or_b32_e32 v166, 32, v164
	v_or_b32_e32 v164, 48, v164
	v_ashrrev_i32_e32 v167, 31, v166
	v_ashrrev_i32_e32 v165, 31, v164
	v_lshlrev_b64 v[182:183], 12, v[166:167]
	v_lshlrev_b64 v[184:185], 12, v[164:165]
	v_lshl_add_u64 v[164:165], s[12:13], 0, v[136:137]
	v_lshl_add_u64 v[168:169], v[134:135], 0, v[182:183]
	v_lshl_add_u64 v[176:177], v[134:135], 0, v[184:185]
	v_lshl_add_u64 v[186:187], v[164:165], 0, v[132:133]
	global_load_dwordx4 v[164:167], v[168:169], off
	s_nop 0
	global_load_dwordx4 v[168:171], v[168:169], off offset:256
	s_nop 0
	global_load_dwordx4 v[172:175], v[176:177], off
	s_nop 0
	global_load_dwordx4 v[176:179], v[176:177], off offset:256
	v_lshl_add_u64 v[248:249], v[134:135], 0, v[136:137]
	v_lshl_add_u64 v[240:241], v[248:249], 0, s[8:9]
	v_lshl_add_u64 v[242:243], v[248:249], 0, s[14:15]
	v_lshl_add_u64 v[244:245], v[248:249], 0, s[16:17]
	v_lshl_add_u64 v[246:247], v[248:249], 0, s[18:19]
	global_load_dwordx4 v[208:211], v[240:241], off
	global_load_dwordx4 v[212:215], v[240:241], off offset:256
	global_load_dwordx4 v[216:219], v[242:243], off
	global_load_dwordx4 v[220:223], v[242:243], off offset:256
	global_load_dwordx4 v[224:227], v[244:245], off
	global_load_dwordx4 v[228:231], v[244:245], off offset:256
	global_load_dwordx4 v[232:235], v[246:247], off
	global_load_dwordx4 v[236:239], v[246:247], off offset:256
	s_andn2_b64 vcc, exec, s[4:5]
	s_mov_b64 s[4:5], -1
	s_waitcnt vmcnt(15)
	v_lshlrev_b32_e32 v188, 16, v148
	v_and_b32_e32 v148, 0xffff0000, v148
	v_lshlrev_b32_e32 v189, 16, v149
	v_and_b32_e32 v149, 0xffff0000, v149
	s_waitcnt vmcnt(13)
	v_lshlrev_b32_e32 v196, 16, v156
	v_and_b32_e32 v156, 0xffff0000, v156
	v_lshlrev_b32_e32 v190, 16, v150
	v_and_b32_e32 v150, 0xffff0000, v150
	v_lshlrev_b32_e32 v191, 16, v151
	v_and_b32_e32 v151, 0xffff0000, v151
	v_lshlrev_b32_e32 v192, 16, v152
	v_and_b32_e32 v152, 0xffff0000, v152
	v_lshlrev_b32_e32 v193, 16, v153
	v_and_b32_e32 v153, 0xffff0000, v153
	v_lshlrev_b32_e32 v197, 16, v157
	v_and_b32_e32 v157, 0xffff0000, v157
	v_add_f32_e32 v116, v116, v188
	v_add_f32_e32 v117, v117, v148
	v_add_f32_e32 v118, v118, v189
	v_add_f32_e32 v119, v119, v149
	v_add_f32_e32 v148, v108, v196
	v_add_f32_e32 v149, v109, v156
	v_cvt_pk_bf16_f32 v108, v116, v117
	v_cvt_pk_bf16_f32 v109, v118, v119
	v_lshlrev_b32_e32 v194, 16, v154
	v_and_b32_e32 v154, 0xffff0000, v154
	v_lshlrev_b32_e32 v195, 16, v155
	v_and_b32_e32 v155, 0xffff0000, v155
	v_lshlrev_b32_e32 v198, 16, v158
	v_add_f32_e32 v112, v112, v190
	v_add_f32_e32 v113, v113, v150
	v_add_f32_e32 v114, v114, v191
	v_add_f32_e32 v115, v115, v151
	v_add_f32_e32 v124, v124, v192
	v_add_f32_e32 v125, v125, v152
	v_add_f32_e32 v126, v126, v193
	v_add_f32_e32 v127, v127, v153
	v_add_f32_e32 v150, v110, v197
	v_add_f32_e32 v151, v111, v157
	v_cvt_pk_bf16_f32 v110, v112, v113
	v_cvt_pk_bf16_f32 v111, v114, v115
	global_store_dwordx4 v[186:187], v[108:111], off
	v_add_f32_e32 v120, v120, v194
	v_add_f32_e32 v121, v121, v154
	v_cvt_pk_bf16_f32 v108, v124, v125
	v_cvt_pk_bf16_f32 v109, v126, v127
	v_add_f32_e32 v122, v122, v195
	v_add_f32_e32 v123, v123, v155
	v_add_f32_e32 v152, v100, v198
	v_cvt_pk_bf16_f32 v110, v120, v121
	v_cvt_pk_bf16_f32 v111, v122, v123
	global_store_dwordx4 v[186:187], v[108:111], off offset:256
	v_and_b32_e32 v100, 0xffff0000, v159
	v_and_b32_e32 v158, 0xffff0000, v158
	v_lshl_add_u64 v[108:109], s[12:13], 0, v[180:181]
	v_lshlrev_b32_e32 v199, 16, v159
	v_add_f32_e32 v103, v103, v100
	v_cvt_pk_bf16_f32 v100, v148, v149
	v_lshl_add_u64 v[108:109], v[108:109], 0, v[132:133]
	v_add_f32_e32 v153, v101, v158
	v_add_f32_e32 v154, v102, v199
	v_cvt_pk_bf16_f32 v101, v150, v151
	v_cvt_pk_bf16_f32 v102, v152, v153
	v_cvt_pk_bf16_f32 v103, v154, v103
	global_store_dwordx4 v[108:109], v[100:103], off
	s_waitcnt vmcnt(15)
	s_nop 0
	v_lshlrev_b32_e32 v100, 16, v160
	v_add_f32_e32 v100, v104, v100
	v_lshlrev_b32_e32 v104, 16, v162
	v_and_b32_e32 v101, 0xffff0000, v160
	v_add_f32_e32 v104, v96, v104
	v_and_b32_e32 v96, 0xffff0000, v162
	v_add_f32_e32 v101, v105, v101
	v_lshlrev_b32_e32 v102, 16, v161
	v_add_f32_e32 v105, v97, v96
	v_lshlrev_b32_e32 v96, 16, v163
	v_add_f32_e32 v102, v106, v102
	v_add_f32_e32 v106, v98, v96
	v_and_b32_e32 v96, 0xffff0000, v163
	v_and_b32_e32 v103, 0xffff0000, v161
	v_add_f32_e32 v99, v99, v96
	v_cvt_pk_bf16_f32 v96, v100, v101
	v_add_f32_e32 v103, v107, v103
	v_cvt_pk_bf16_f32 v97, v102, v103
	v_cvt_pk_bf16_f32 v98, v104, v105
	v_cvt_pk_bf16_f32 v99, v106, v99
	global_store_dwordx4 v[108:109], v[96:99], off offset:256
	v_lshl_add_u64 v[100:101], v[136:137], 0, s[16:17]
	v_lshl_add_u64 v[102:103], v[136:137], 0, s[18:19]
	s_waitcnt vmcnt(15)
	v_lshlrev_b32_e32 v96, 16, v164
	v_add_f32_e32 v92, v92, v96
	v_and_b32_e32 v96, 0xffff0000, v164
	v_add_f32_e32 v93, v93, v96
	v_lshlrev_b32_e32 v96, 16, v165
	v_add_f32_e32 v94, v94, v96
	v_and_b32_e32 v96, 0xffff0000, v165
	v_add_f32_e32 v95, v95, v96
	v_lshlrev_b32_e32 v96, 16, v166
	v_add_f32_e32 v96, v84, v96
	v_and_b32_e32 v84, 0xffff0000, v166
	v_add_f32_e32 v97, v85, v84
	v_lshlrev_b32_e32 v84, 16, v167
	v_add_f32_e32 v98, v86, v84
	v_and_b32_e32 v84, 0xffff0000, v167
	v_add_f32_e32 v87, v87, v84
	v_cvt_pk_bf16_f32 v84, v92, v93
	v_lshl_add_u64 v[92:93], s[12:13], 0, v[182:183]
	v_lshl_add_u64 v[92:93], v[92:93], 0, v[132:133]
	v_cvt_pk_bf16_f32 v85, v94, v95
	v_cvt_pk_bf16_f32 v86, v96, v97
	v_cvt_pk_bf16_f32 v87, v98, v87
	global_store_dwordx4 v[92:93], v[84:87], off
	v_lshl_add_u64 v[96:97], v[136:137], 0, s[8:9]
	v_lshl_add_u64 v[98:99], v[136:137], 0, s[14:15]
	s_waitcnt vmcnt(15)
	v_lshlrev_b32_e32 v84, 16, v168
	v_add_f32_e32 v84, v88, v84
	v_lshlrev_b32_e32 v88, 16, v170
	v_and_b32_e32 v85, 0xffff0000, v168
	v_add_f32_e32 v88, v80, v88
	v_and_b32_e32 v80, 0xffff0000, v170
	v_add_f32_e32 v85, v89, v85
	v_lshlrev_b32_e32 v86, 16, v169
	v_add_f32_e32 v89, v81, v80
	v_lshlrev_b32_e32 v80, 16, v171
	v_add_f32_e32 v86, v90, v86
	v_add_f32_e32 v90, v82, v80
	v_and_b32_e32 v80, 0xffff0000, v171
	v_and_b32_e32 v87, 0xffff0000, v169
	v_add_f32_e32 v83, v83, v80
	v_cvt_pk_bf16_f32 v80, v84, v85
	v_add_f32_e32 v87, v91, v87
	v_cvt_pk_bf16_f32 v81, v86, v87
	v_cvt_pk_bf16_f32 v82, v88, v89
	v_cvt_pk_bf16_f32 v83, v90, v83
	global_store_dwordx4 v[92:93], v[80:83], off offset:256
	v_lshl_add_u64 v[84:85], v[134:135], 0, v[100:101]
	v_lshl_add_u64 v[92:93], v[134:135], 0, v[102:103]
	s_waitcnt vmcnt(15)
	v_lshlrev_b32_e32 v80, 16, v172
	v_add_f32_e32 v72, v72, v80
	v_and_b32_e32 v80, 0xffff0000, v172
	v_add_f32_e32 v73, v73, v80
	v_lshlrev_b32_e32 v80, 16, v173
	v_add_f32_e32 v74, v74, v80
	v_and_b32_e32 v80, 0xffff0000, v173
	v_add_f32_e32 v75, v75, v80
	v_lshlrev_b32_e32 v80, 16, v174
	v_add_f32_e32 v80, v56, v80
	v_and_b32_e32 v56, 0xffff0000, v174
	v_add_f32_e32 v81, v57, v56
	v_lshlrev_b32_e32 v56, 16, v175
	v_add_f32_e32 v82, v58, v56
	v_and_b32_e32 v56, 0xffff0000, v175
	v_add_f32_e32 v59, v59, v56
	v_cvt_pk_bf16_f32 v56, v72, v73
	v_lshl_add_u64 v[72:73], s[12:13], 0, v[184:185]
	v_lshl_add_u64 v[72:73], v[72:73], 0, v[132:133]
	v_cvt_pk_bf16_f32 v57, v74, v75
	v_cvt_pk_bf16_f32 v58, v80, v81
	v_cvt_pk_bf16_f32 v59, v82, v59
	global_store_dwordx4 v[72:73], v[56:59], off
	s_waitcnt vmcnt(15)
	s_nop 0
	v_lshlrev_b32_e32 v56, 16, v176
	v_add_f32_e32 v56, v64, v56
	v_lshlrev_b32_e32 v64, 16, v178
	v_and_b32_e32 v57, 0xffff0000, v176
	v_add_f32_e32 v64, v48, v64
	v_and_b32_e32 v48, 0xffff0000, v178
	v_add_f32_e32 v57, v65, v57
	v_lshlrev_b32_e32 v58, 16, v177
	v_add_f32_e32 v65, v49, v48
	v_lshlrev_b32_e32 v48, 16, v179
	v_add_f32_e32 v58, v66, v58
	v_add_f32_e32 v66, v50, v48
	v_and_b32_e32 v48, 0xffff0000, v179
	v_and_b32_e32 v59, 0xffff0000, v177
	v_add_f32_e32 v51, v51, v48
	v_add_f32_e32 v59, v67, v59
	v_cvt_pk_bf16_f32 v48, v56, v57
	v_cvt_pk_bf16_f32 v49, v58, v59
	v_cvt_pk_bf16_f32 v50, v64, v65
	v_cvt_pk_bf16_f32 v51, v66, v51
	global_store_dwordx4 v[72:73], v[48:51], off offset:256
	v_lshl_add_u64 v[56:57], v[134:135], 0, v[96:97]
	s_waitcnt vmcnt(8)
	v_mov_b32_e32 v48, v208
	v_mov_b32_e32 v49, v209
	v_mov_b32_e32 v50, v210
	v_mov_b32_e32 v51, v211
	s_nop 0
	v_mov_b32_e32 v56, v212
	v_mov_b32_e32 v57, v213
	v_mov_b32_e32 v58, v214
	v_mov_b32_e32 v59, v215
	v_lshl_add_u64 v[72:73], v[134:135], 0, v[98:99]
	v_mov_b32_e32 v64, v216
	v_mov_b32_e32 v65, v217
	v_mov_b32_e32 v66, v218
	v_mov_b32_e32 v67, v219
	s_nop 0
	v_mov_b32_e32 v72, v220
	v_mov_b32_e32 v73, v221
	v_mov_b32_e32 v74, v222
	v_mov_b32_e32 v75, v223
	s_nop 0
	v_mov_b32_e32 v80, v224
	v_mov_b32_e32 v81, v225
	v_mov_b32_e32 v82, v226
	v_mov_b32_e32 v83, v227
	s_nop 0
	v_mov_b32_e32 v84, v228
	v_mov_b32_e32 v85, v229
	v_mov_b32_e32 v86, v230
	v_mov_b32_e32 v87, v231
	s_nop 0
	v_mov_b32_e32 v88, v232
	v_mov_b32_e32 v89, v233
	v_mov_b32_e32 v90, v234
	v_mov_b32_e32 v91, v235
	s_nop 0
	v_mov_b32_e32 v92, v236
	v_mov_b32_e32 v93, v237
	v_mov_b32_e32 v94, v238
	v_mov_b32_e32 v95, v239
	v_lshlrev_b32_e32 v104, 16, v48
	v_and_b32_e32 v48, 0xffff0000, v48
	v_add_f32_e32 v48, v77, v48
	v_lshlrev_b32_e32 v77, 16, v49
	v_add_f32_e32 v77, v78, v77
	v_lshlrev_b32_e32 v78, 16, v50
	v_and_b32_e32 v50, 0xffff0000, v50
	v_and_b32_e32 v49, 0xffff0000, v49
	v_add_f32_e32 v50, v61, v50
	v_lshlrev_b32_e32 v61, 16, v51
	v_and_b32_e32 v51, 0xffff0000, v51
	v_add_f32_e32 v49, v79, v49
	v_add_f32_e32 v60, v60, v78
	v_add_f32_e32 v61, v62, v61
	v_add_f32_e32 v51, v63, v51
	v_add_f32_e32 v76, v76, v104
	v_cvt_pk_bf16_f32 v48, v76, v48
	v_cvt_pk_bf16_f32 v49, v77, v49
	v_cvt_pk_bf16_f32 v50, v60, v50
	v_cvt_pk_bf16_f32 v51, v61, v51
	v_lshl_add_u64 v[60:61], s[12:13], 0, v[96:97]
	v_lshl_add_u64 v[60:61], v[60:61], 0, v[132:133]
	global_store_dwordx4 v[60:61], v[48:51], off
	s_nop 0
	v_lshlrev_b32_e32 v48, 16, v56
	v_and_b32_e32 v49, 0xffff0000, v56
	v_lshlrev_b32_e32 v56, 16, v58
	v_add_f32_e32 v52, v52, v56
	v_and_b32_e32 v56, 0xffff0000, v58
	v_add_f32_e32 v48, v68, v48
	v_lshlrev_b32_e32 v50, 16, v57
	v_and_b32_e32 v51, 0xffff0000, v57
	v_add_f32_e32 v53, v53, v56
	v_lshlrev_b32_e32 v56, 16, v59
	v_add_f32_e32 v49, v69, v49
	v_add_f32_e32 v50, v70, v50
	v_add_f32_e32 v51, v71, v51
	v_add_f32_e32 v54, v54, v56
	v_and_b32_e32 v56, 0xffff0000, v59
	v_cvt_pk_bf16_f32 v48, v48, v49
	v_add_f32_e32 v55, v55, v56
	v_cvt_pk_bf16_f32 v49, v50, v51
	v_cvt_pk_bf16_f32 v50, v52, v53
	v_cvt_pk_bf16_f32 v51, v54, v55
	global_store_dwordx4 v[60:61], v[48:51], off offset:256
	s_nop 0
	v_lshlrev_b32_e32 v48, 16, v64
	v_add_f32_e32 v44, v44, v48
	v_and_b32_e32 v48, 0xffff0000, v64
	v_add_f32_e32 v45, v45, v48
	v_lshlrev_b32_e32 v48, 16, v65
	v_add_f32_e32 v46, v46, v48
	v_and_b32_e32 v48, 0xffff0000, v65
	v_add_f32_e32 v47, v47, v48
	v_lshlrev_b32_e32 v48, 16, v66
	v_add_f32_e32 v48, v36, v48
	v_and_b32_e32 v36, 0xffff0000, v66
	v_add_f32_e32 v49, v37, v36
	v_lshlrev_b32_e32 v36, 16, v67
	v_add_f32_e32 v50, v38, v36
	v_and_b32_e32 v36, 0xffff0000, v67
	v_add_f32_e32 v39, v39, v36
	v_cvt_pk_bf16_f32 v36, v44, v45
	v_lshl_add_u64 v[44:45], s[12:13], 0, v[98:99]
	v_lshl_add_u64 v[44:45], v[44:45], 0, v[132:133]
	v_cvt_pk_bf16_f32 v37, v46, v47
	v_cvt_pk_bf16_f32 v38, v48, v49
	v_cvt_pk_bf16_f32 v39, v50, v39
	global_store_dwordx4 v[44:45], v[36:39], off
	s_nop 0
	v_lshlrev_b32_e32 v36, 16, v72
	v_add_f32_e32 v36, v40, v36
	v_lshlrev_b32_e32 v40, 16, v74
	v_and_b32_e32 v37, 0xffff0000, v72
	v_add_f32_e32 v40, v32, v40
	v_and_b32_e32 v32, 0xffff0000, v74
	v_add_f32_e32 v37, v41, v37
	v_lshlrev_b32_e32 v38, 16, v73
	v_add_f32_e32 v41, v33, v32
	v_lshlrev_b32_e32 v32, 16, v75
	v_add_f32_e32 v38, v42, v38
	v_add_f32_e32 v42, v34, v32
	v_and_b32_e32 v32, 0xffff0000, v75
	v_and_b32_e32 v39, 0xffff0000, v73
	v_add_f32_e32 v35, v35, v32
	v_cvt_pk_bf16_f32 v32, v36, v37
	v_add_f32_e32 v39, v43, v39
	v_cvt_pk_bf16_f32 v33, v38, v39
	v_cvt_pk_bf16_f32 v34, v40, v41
	v_cvt_pk_bf16_f32 v35, v42, v35
	global_store_dwordx4 v[44:45], v[32:35], off offset:256
	s_nop 0
	v_lshlrev_b32_e32 v32, 16, v80
	v_add_f32_e32 v28, v28, v32
	v_and_b32_e32 v32, 0xffff0000, v80
	v_add_f32_e32 v29, v29, v32
	v_lshlrev_b32_e32 v32, 16, v81
	v_add_f32_e32 v30, v30, v32
	v_and_b32_e32 v32, 0xffff0000, v81
	v_add_f32_e32 v31, v31, v32
	v_lshlrev_b32_e32 v32, 16, v82
	v_add_f32_e32 v32, v20, v32
	v_and_b32_e32 v20, 0xffff0000, v82
	v_add_f32_e32 v33, v21, v20
	v_lshlrev_b32_e32 v20, 16, v83
	v_add_f32_e32 v34, v22, v20
	v_and_b32_e32 v20, 0xffff0000, v83
	v_add_f32_e32 v23, v23, v20
	v_cvt_pk_bf16_f32 v20, v28, v29
	v_lshl_add_u64 v[28:29], s[12:13], 0, v[100:101]
	v_lshl_add_u64 v[28:29], v[28:29], 0, v[132:133]
	v_cvt_pk_bf16_f32 v21, v30, v31
	v_cvt_pk_bf16_f32 v22, v32, v33
	v_cvt_pk_bf16_f32 v23, v34, v23
	global_store_dwordx4 v[28:29], v[20:23], off
	s_nop 0
	v_lshlrev_b32_e32 v20, 16, v84
	v_add_f32_e32 v20, v24, v20
	v_lshlrev_b32_e32 v24, 16, v86
	v_and_b32_e32 v21, 0xffff0000, v84
	v_add_f32_e32 v24, v16, v24
	v_and_b32_e32 v16, 0xffff0000, v86
	v_add_f32_e32 v21, v25, v21
	v_lshlrev_b32_e32 v22, 16, v85
	v_add_f32_e32 v25, v17, v16
	v_lshlrev_b32_e32 v16, 16, v87
	v_add_f32_e32 v22, v26, v22
	v_add_f32_e32 v26, v18, v16
	v_and_b32_e32 v16, 0xffff0000, v87
	v_and_b32_e32 v23, 0xffff0000, v85
	v_add_f32_e32 v19, v19, v16
	v_cvt_pk_bf16_f32 v16, v20, v21
	v_add_f32_e32 v23, v27, v23
	v_cvt_pk_bf16_f32 v17, v22, v23
	v_cvt_pk_bf16_f32 v18, v24, v25
	v_cvt_pk_bf16_f32 v19, v26, v19
	global_store_dwordx4 v[28:29], v[16:19], off offset:256
	s_nop 0
	v_lshlrev_b32_e32 v16, 16, v88
	v_add_f32_e32 v12, v12, v16
	v_and_b32_e32 v16, 0xffff0000, v88
	v_add_f32_e32 v13, v13, v16
	v_lshlrev_b32_e32 v16, 16, v89
	v_add_f32_e32 v14, v14, v16
	v_and_b32_e32 v16, 0xffff0000, v89
	v_add_f32_e32 v15, v15, v16
	v_lshlrev_b32_e32 v16, 16, v90
	v_add_f32_e32 v16, v4, v16
	v_and_b32_e32 v4, 0xffff0000, v90
	v_add_f32_e32 v17, v5, v4
	v_lshlrev_b32_e32 v4, 16, v91
	v_add_f32_e32 v18, v6, v4
	v_and_b32_e32 v4, 0xffff0000, v91
	v_add_f32_e32 v7, v7, v4
	v_cvt_pk_bf16_f32 v4, v12, v13
	v_lshl_add_u64 v[12:13], s[12:13], 0, v[102:103]
	v_lshl_add_u64 v[12:13], v[12:13], 0, v[132:133]
	v_cvt_pk_bf16_f32 v5, v14, v15
	v_cvt_pk_bf16_f32 v6, v16, v17
	v_cvt_pk_bf16_f32 v7, v18, v7
	global_store_dwordx4 v[12:13], v[4:7], off
	s_nop 0
	v_lshlrev_b32_e32 v4, 16, v92
	v_add_f32_e32 v4, v8, v4
	v_lshlrev_b32_e32 v8, 16, v94
	v_and_b32_e32 v5, 0xffff0000, v92
	v_add_f32_e32 v8, v0, v8
	v_and_b32_e32 v0, 0xffff0000, v94
	v_add_f32_e32 v5, v9, v5
	v_lshlrev_b32_e32 v6, 16, v93
	v_add_f32_e32 v9, v1, v0
	v_lshlrev_b32_e32 v0, 16, v95
	v_add_f32_e32 v6, v10, v6
	v_add_f32_e32 v10, v2, v0
	v_and_b32_e32 v0, 0xffff0000, v95
	v_and_b32_e32 v7, 0xffff0000, v93
	v_add_f32_e32 v3, v3, v0
	v_add_f32_e32 v7, v11, v7
	v_cvt_pk_bf16_f32 v0, v4, v5
	v_cvt_pk_bf16_f32 v1, v6, v7
	v_cvt_pk_bf16_f32 v2, v8, v9
	v_cvt_pk_bf16_f32 v3, v10, v3
	global_store_dwordx4 v[12:13], v[0:3], off offset:256
	s_cbranch_vccnz .LBB0_1101
	s_andn2_b64 vcc, exec, s[6:7]
	s_cbranch_vccnz .LBB0_1100
	s_barrier
	s_branch .LBB0_1100
